# speedup vs baseline: 1.0102x; 1.0102x over previous
.LBB2_76:
	s_cmp_gt_u32 s35, 13
	v_lshl_add_u64 v[158:159], v[230:231], 0, s[6:7]
	v_lshl_add_u64 v[160:161], v[222:223], 0, s[6:7]
	v_lshl_add_u64 v[156:157], v[224:225], 0, s[6:7]
	v_lshl_add_u64 v[154:155], v[226:227], 0, s[6:7]
	s_barrier
	s_waitcnt lgkmcnt(0)
	ds_read_b128 v[38:41], v201 offset:18432
	ds_read_b128 v[42:45], v201 offset:20480
	ds_read_b128 v[6:9], v205
	ds_read_b128 v[14:17], v205 offset:2048
	ds_read_b128 v[22:25], v205 offset:4096
	ds_read_b128 v[30:33], v205 offset:6144
	ds_read_b128 v[46:49], v205 offset:8192
	ds_read_b128 v[50:53], v205 offset:10240
	s_cbranch_scc1 .LBB2_79
	v_add_u32_e32 v4, s36, v1
	v_add_u32_e32 v5, 0x2000, v4
	v_readfirstlane_b32 s0, v4
	v_lshl_add_u64 v[2:3], v[158:159], 0, s[12:13]
	s_mov_b32 m0, s0
	v_readfirstlane_b32 s0, v5
	v_add_u32_e32 v5, 0x4000, v4
	global_load_lds_dwordx4 v[2:3], off
	v_lshl_add_u64 v[2:3], v[158:159], 0, s[14:15]
	s_mov_b32 m0, s0
	v_readfirstlane_b32 s0, v5
	v_add_u32_e32 v4, 0x6000, v4
	global_load_lds_dwordx4 v[2:3], off
	v_lshl_add_u64 v[2:3], v[160:161], 0, s[12:13]
	s_mov_b32 m0, s0
	v_readfirstlane_b32 s0, v4
	v_add_u32_e32 v4, s37, v1
	global_load_lds_dwordx4 v[2:3], off
	v_lshl_add_u64 v[2:3], v[158:159], 0, s[16:17]
	s_mov_b32 m0, s0
	v_readfirstlane_b32 s0, v4
	v_add_u32_e32 v4, 0x2000, v4
	global_load_lds_dwordx4 v[2:3], off
	v_lshl_add_u64 v[2:3], v[156:157], 0, s[12:13]
	s_mov_b32 m0, s0
	v_readfirstlane_b32 s0, v4
	global_load_lds_dwordx4 v[2:3], off
	v_lshl_add_u64 v[2:3], v[154:155], 0, s[12:13]
	s_mov_b32 m0, s0
	s_and_b64 vcc, exec, s[2:3]
	global_load_lds_dwordx4 v[2:3], off
	s_cbranch_vccnz .LBB2_79
	v_add_u32_e32 v4, s38, v1
	v_lshl_add_u64 v[2:3], v[228:229], 0, s[6:7]
	v_readfirstlane_b32 s0, v4
	v_lshl_add_u64 v[2:3], v[2:3], 0, s[12:13]
	s_mov_b32 m0, s0
	s_nop 0
	global_load_lds_dwordx4 v[2:3], off
.LBB2_79:
	s_andn2_b64 vcc, exec, s[10:11]
	s_waitcnt lgkmcnt(0)
	v_mfma_f32_16x16x32_f16 v[34:37], v[38:41], v[46:49], v[106:109]
	v_mfma_f32_16x16x32_f16 v[102:105], v[42:45], v[46:49], v[102:105]
	v_mfma_f32_16x16x32_f16 v[98:101], v[38:41], v[50:53], v[98:101]
	v_mfma_f32_16x16x32_f16 v[94:97], v[42:45], v[50:53], v[94:97]
	ds_read_b128 v[46:49], v205 offset:12288
	ds_read_b128 v[50:53], v205 offset:14336
	v_mfma_f32_16x16x32_f16 v[2:5], v[38:41], v[6:9], v[138:141]
	v_mfma_f32_16x16x32_f16 v[6:9], v[42:45], v[6:9], v[134:137]
	v_mfma_f32_16x16x32_f16 v[10:13], v[38:41], v[14:17], v[130:133]
	v_mfma_f32_16x16x32_f16 v[14:17], v[42:45], v[14:17], v[126:129]
	v_mfma_f32_16x16x32_f16 v[18:21], v[38:41], v[22:25], v[122:125]
	v_mfma_f32_16x16x32_f16 v[22:25], v[42:45], v[22:25], v[118:121]
	v_mfma_f32_16x16x32_f16 v[26:29], v[38:41], v[30:33], v[114:117]
	v_mfma_f32_16x16x32_f16 v[30:33], v[42:45], v[30:33], v[110:113]
	s_waitcnt lgkmcnt(0)
	v_mfma_f32_16x16x32_f16 v[90:93], v[38:41], v[46:49], v[90:93]
	v_mfma_f32_16x16x32_f16 v[86:89], v[42:45], v[46:49], v[86:89]
	v_cndmask_b32_e64 v46, 0, 1, s[10:11]
	v_cmp_ne_u32_e64 s[0:1], 1, v46
	v_mfma_f32_16x16x32_f16 v[106:109], v[38:41], v[50:53], v[142:145]
	v_mfma_f32_16x16x32_f16 v[82:85], v[42:45], v[50:53], v[82:85]
	s_cbranch_vccnz .LBB2_81
	ds_read_b128 v[46:49], v205 offset:16384
	s_waitcnt lgkmcnt(0)
	v_mfma_f32_16x16x32_f16 v[70:73], v[38:41], v[46:49], v[70:73]
	v_mfma_f32_16x16x32_f16 v[78:81], v[42:45], v[46:49], v[78:81]
.LBB2_81:
	s_waitcnt lgkmcnt(0)
	ds_read_b128 v[110:113], v203 offset:18432
	ds_read_b128 v[114:117], v203 offset:20480
	ds_read_b128 v[38:41], v207
	ds_read_b128 v[42:45], v207 offset:2048
	ds_read_b128 v[232:235], v207 offset:4096
	ds_read_b128 v[236:239], v207 offset:6144
	ds_read_b128 v[240:243], v207 offset:8192
	ds_read_b128 v[244:247], v207 offset:10240
	s_and_b64 vcc, exec, s[0:1]
	s_waitcnt lgkmcnt(5)
	v_mfma_f32_16x16x32_f16 v[74:77], v[110:113], v[38:41], v[2:5]
	v_mfma_f32_16x16x32_f16 v[66:69], v[114:117], v[38:41], v[6:9]
	s_waitcnt lgkmcnt(4)
	v_mfma_f32_16x16x32_f16 v[62:65], v[110:113], v[42:45], v[10:13]
	v_mfma_f32_16x16x32_f16 v[58:61], v[114:117], v[42:45], v[14:17]
	s_waitcnt lgkmcnt(3)
	v_mfma_f32_16x16x32_f16 v[54:57], v[110:113], v[232:235], v[18:21]
	v_mfma_f32_16x16x32_f16 v[50:53], v[114:117], v[232:235], v[22:25]
	ds_read_b128 v[232:235], v207 offset:12288
	s_waitcnt lgkmcnt(3)
	v_mfma_f32_16x16x32_f16 v[46:49], v[110:113], v[236:239], v[26:29]
	v_mfma_f32_16x16x32_f16 v[42:45], v[114:117], v[236:239], v[30:33]
	ds_read_b128 v[236:239], v207 offset:14336
	s_waitcnt lgkmcnt(3)
	v_mfma_f32_16x16x32_f16 v[38:41], v[110:113], v[240:243], v[34:37]
	v_mfma_f32_16x16x32_f16 v[34:37], v[114:117], v[240:243], v[102:105]
	s_waitcnt lgkmcnt(2)
	v_mfma_f32_16x16x32_f16 v[30:33], v[110:113], v[244:247], v[98:101]
	v_mfma_f32_16x16x32_f16 v[26:29], v[114:117], v[244:247], v[94:97]
	s_waitcnt lgkmcnt(1)
	v_mfma_f32_16x16x32_f16 v[22:25], v[110:113], v[232:235], v[90:93]
	v_mfma_f32_16x16x32_f16 v[18:21], v[114:117], v[232:235], v[86:89]
	s_waitcnt lgkmcnt(0)
	v_mfma_f32_16x16x32_f16 v[14:17], v[110:113], v[236:239], v[106:109]
	v_mfma_f32_16x16x32_f16 v[10:13], v[114:117], v[236:239], v[82:85]
	s_cbranch_vccnz .LBB2_83
	ds_read_b128 v[2:5], v207 offset:16384
	s_waitcnt lgkmcnt(0)
	v_mfma_f32_16x16x32_f16 v[6:9], v[110:113], v[2:5], v[70:73]
	v_mfma_f32_16x16x32_f16 v[2:5], v[114:117], v[2:5], v[78:81]
	s_andn2_b64 vcc, exec, s[30:31]
	s_mov_b64 s[30:31], -1
	s_cbranch_vccnz .LBB2_67
	s_branch .LBB2_84

.LBB2_92:
	s_cmp_gt_u32 s35, 12
	s_barrier
	s_waitcnt lgkmcnt(0)
	v_add_u32_e32 v70, 0, v195
	ds_read_b128 v[146:149], v70 offset:51200
	ds_read_b128 v[150:153], v70 offset:53248
	ds_read_b128 v[70:73], v205 offset:51200
	ds_read_b128 v[78:81], v205 offset:53248
	ds_read_b128 v[232:235], v205 offset:55296
	ds_read_b128 v[236:239], v205 offset:57344
	s_cbranch_scc1 .LBB2_95
	v_add_u32_e32 v250, 0x4800, v187
	v_lshl_add_u64 v[248:249], v[158:159], 0, s[18:19]
	v_readfirstlane_b32 s30, v250
	v_add_u32_e32 v250, 0x6800, v187
	s_mov_b32 m0, s30
	v_readfirstlane_b32 s30, v250
	v_add_u32_e32 v250, 0x8800, v187
	global_load_lds_dwordx4 v[248:249], off
	v_lshl_add_u64 v[248:249], v[158:159], 0, s[20:21]
	s_mov_b32 m0, s30
	v_readfirstlane_b32 s30, v250
	v_add_u32_e32 v250, 0xa800, v187
	global_load_lds_dwordx4 v[248:249], off
	v_lshl_add_u64 v[248:249], v[160:161], 0, s[18:19]
	s_mov_b32 m0, s30
	v_readfirstlane_b32 s30, v250
	global_load_lds_dwordx4 v[248:249], off
	v_lshl_add_u64 v[248:249], v[158:159], 0, s[22:23]
	s_mov_b32 m0, s30
	v_readfirstlane_b32 s30, v187
	v_add_u32_e32 v250, 0x2000, v187
	global_load_lds_dwordx4 v[248:249], off
	v_lshl_add_u64 v[248:249], v[156:157], 0, s[18:19]
	s_mov_b32 m0, s30
	v_readfirstlane_b32 s30, v250
	global_load_lds_dwordx4 v[248:249], off
	v_lshl_add_u64 v[248:249], v[154:155], 0, s[18:19]
	s_mov_b32 m0, s30
	s_and_b64 vcc, exec, s[2:3]
	global_load_lds_dwordx4 v[248:249], off
	s_cbranch_vccnz .LBB2_95
	v_add_u32_e32 v250, 0x4000, v187
	v_lshl_add_u64 v[248:249], v[228:229], 0, s[6:7]
	v_readfirstlane_b32 s30, v250
	v_lshl_add_u64 v[248:249], v[248:249], 0, s[18:19]
	s_mov_b32 m0, s30
	s_nop 0
	global_load_lds_dwordx4 v[248:249], off
.LBB2_95:
	s_and_b64 vcc, exec, s[0:1]
	s_waitcnt lgkmcnt(2)
	v_mfma_f32_16x16x32_f16 v[82:85], v[146:149], v[70:73], v[74:77]
	v_mfma_f32_16x16x32_f16 v[86:89], v[150:153], v[70:73], v[66:69]
	v_mfma_f32_16x16x32_f16 v[90:93], v[146:149], v[78:81], v[62:65]
	v_mfma_f32_16x16x32_f16 v[94:97], v[150:153], v[78:81], v[58:61]
	ds_read_b128 v[240:243], v205 offset:59392
	ds_read_b128 v[244:247], v205 offset:61440
	s_waitcnt lgkmcnt(2)
	v_mfma_f32_16x16x32_f16 v[98:101], v[146:149], v[232:235], v[54:57]
	v_mfma_f32_16x16x32_f16 v[102:105], v[150:153], v[232:235], v[50:53]
	v_mfma_f32_16x16x32_f16 v[106:109], v[146:149], v[236:239], v[46:49]
	v_mfma_f32_16x16x32_f16 v[110:113], v[150:153], v[236:239], v[42:45]
	ds_read_b128 v[232:235], v205 offset:63488
	ds_read_b128 v[236:239], v209 offset:14336
	s_waitcnt lgkmcnt(2)
	v_mfma_f32_16x16x32_f16 v[114:117], v[146:149], v[240:243], v[38:41]
	v_mfma_f32_16x16x32_f16 v[118:121], v[150:153], v[240:243], v[34:37]
	v_mfma_f32_16x16x32_f16 v[122:125], v[146:149], v[244:247], v[30:33]
	v_mfma_f32_16x16x32_f16 v[126:129], v[150:153], v[244:247], v[26:29]
	v_mov_b64_e32 v[80:81], v[4:5]
	v_mov_b64_e32 v[78:79], v[2:3]
	s_waitcnt lgkmcnt(0)
	v_mfma_f32_16x16x32_f16 v[130:133], v[146:149], v[232:235], v[22:25]
	v_mfma_f32_16x16x32_f16 v[134:137], v[150:153], v[232:235], v[18:21]
	v_mov_b64_e32 v[72:73], v[8:9]
	v_mov_b64_e32 v[70:71], v[6:7]
	v_mfma_f32_16x16x32_f16 v[138:141], v[146:149], v[236:239], v[14:17]
	v_mfma_f32_16x16x32_f16 v[142:145], v[150:153], v[236:239], v[10:13]
	s_cbranch_vccnz .LBB2_97
	ds_read_b128 v[78:81], v209 offset:16384
	s_waitcnt lgkmcnt(0)
	v_mfma_f32_16x16x32_f16 v[70:73], v[146:149], v[78:81], v[6:9]
	v_mfma_f32_16x16x32_f16 v[78:81], v[150:153], v[78:81], v[2:5]
.LBB2_97:
	s_waitcnt lgkmcnt(0)
	v_add_u32_e32 v150, 0, v199
	ds_read_b128 v[146:149], v150 offset:51200
	ds_read_b128 v[150:153], v150 offset:53248
	ds_read_b128 v[162:165], v207 offset:51200
	ds_read_b128 v[166:169], v207 offset:53248
	ds_read_b128 v[232:235], v207 offset:55296
	ds_read_b128 v[236:239], v207 offset:57344
	ds_read_b128 v[240:243], v207 offset:59392
	ds_read_b128 v[244:247], v207 offset:61440
	s_and_b64 vcc, exec, s[0:1]
	s_waitcnt lgkmcnt(5)
	v_mfma_f32_16x16x32_f16 v[82:85], v[146:149], v[162:165], v[82:85]
	v_mfma_f32_16x16x32_f16 v[86:89], v[150:153], v[162:165], v[86:89]
	s_waitcnt lgkmcnt(4)
	v_mfma_f32_16x16x32_f16 v[90:93], v[146:149], v[166:169], v[90:93]
	v_mfma_f32_16x16x32_f16 v[94:97], v[150:153], v[166:169], v[94:97]
	s_waitcnt lgkmcnt(3)
	v_mfma_f32_16x16x32_f16 v[98:101], v[146:149], v[232:235], v[98:101]
	v_mfma_f32_16x16x32_f16 v[102:105], v[150:153], v[232:235], v[102:105]
	ds_read_b128 v[232:235], v207 offset:63488
	s_waitcnt lgkmcnt(3)
	v_mfma_f32_16x16x32_f16 v[106:109], v[146:149], v[236:239], v[106:109]
	v_mfma_f32_16x16x32_f16 v[110:113], v[150:153], v[236:239], v[110:113]
	ds_read_b128 v[236:239], v211 offset:14336
	s_waitcnt lgkmcnt(3)
	v_mfma_f32_16x16x32_f16 v[114:117], v[146:149], v[240:243], v[114:117]
	v_mfma_f32_16x16x32_f16 v[118:121], v[150:153], v[240:243], v[118:121]
	s_waitcnt lgkmcnt(2)
	v_mfma_f32_16x16x32_f16 v[122:125], v[146:149], v[244:247], v[122:125]
	v_mfma_f32_16x16x32_f16 v[126:129], v[150:153], v[244:247], v[126:129]
	s_waitcnt lgkmcnt(1)
	v_mfma_f32_16x16x32_f16 v[130:133], v[146:149], v[232:235], v[130:133]
	v_mfma_f32_16x16x32_f16 v[134:137], v[150:153], v[232:235], v[134:137]
	s_waitcnt lgkmcnt(0)
	v_mfma_f32_16x16x32_f16 v[138:141], v[146:149], v[236:239], v[138:141]
	v_mfma_f32_16x16x32_f16 v[142:145], v[150:153], v[236:239], v[142:145]
	s_cbranch_vccnz .LBB2_108
	ds_read_b128 v[162:165], v211 offset:16384
	s_waitcnt lgkmcnt(0)
	v_mfma_f32_16x16x32_f16 v[70:73], v[146:149], v[162:165], v[70:73]
	v_mfma_f32_16x16x32_f16 v[78:81], v[150:153], v[162:165], v[78:81]
	s_cmpk_lg_i32 s6, 0x680
	s_mov_b64 s[30:31], -1
	s_cbranch_scc1 .LBB2_109

.LBB2_101:
	s_cmp_gt_u32 s35, 11
	s_barrier
	s_waitcnt lgkmcnt(0)
	v_add_u32_e32 v146, s37, v195
	ds_read_b128 v[178:181], v146
	ds_read_b128 v[182:185], v146 offset:2048
	v_add_u32_e32 v213, s37, v193
	ds_read_b128 v[146:149], v213
	ds_read_b128 v[150:153], v213 offset:2048
	ds_read_b128 v[232:235], v213 offset:4096
	ds_read_b128 v[236:239], v213 offset:6144
	ds_read_b128 v[240:243], v213 offset:8192
	ds_read_b128 v[244:247], v213 offset:10240
	s_cbranch_scc1 .LBB2_104
	v_readfirstlane_b32 s30, v189
	v_add_u32_e32 v250, 0x2000, v189
	v_lshl_add_u64 v[248:249], v[158:159], 0, s[24:25]
	s_mov_b32 m0, s30
	v_readfirstlane_b32 s30, v250
	v_add_u32_e32 v250, 0x4000, v189
	global_load_lds_dwordx4 v[248:249], off
	v_lshl_add_u64 v[248:249], v[158:159], 0, s[26:27]
	s_mov_b32 m0, s30
	v_readfirstlane_b32 s30, v250
	v_add_u32_e32 v250, 0x6000, v189
	global_load_lds_dwordx4 v[248:249], off
	v_lshl_add_u64 v[248:249], v[160:161], 0, s[24:25]
	s_mov_b32 m0, s30
	v_readfirstlane_b32 s30, v250
	v_add_u32_e32 v250, 0xc800, v187
	global_load_lds_dwordx4 v[248:249], off
	v_lshl_add_u64 v[248:249], v[158:159], 0, s[28:29]
	s_mov_b32 m0, s30
	v_readfirstlane_b32 s30, v250
	v_add_u32_e32 v250, 0xe800, v187
	global_load_lds_dwordx4 v[248:249], off
	v_lshl_add_u64 v[248:249], v[156:157], 0, s[24:25]
	s_mov_b32 m0, s30
	v_readfirstlane_b32 s30, v250
	global_load_lds_dwordx4 v[248:249], off
	v_lshl_add_u64 v[248:249], v[154:155], 0, s[24:25]
	s_mov_b32 m0, s30
	s_and_b64 vcc, exec, s[2:3]
	global_load_lds_dwordx4 v[248:249], off
	s_cbranch_vccnz .LBB2_104
	v_add_u32_e32 v250, s39, v1
	v_lshl_add_u64 v[248:249], v[228:229], 0, s[6:7]
	v_readfirstlane_b32 s30, v250
	v_lshl_add_u64 v[248:249], v[248:249], 0, s[24:25]
	s_mov_b32 m0, s30
	s_nop 0
	global_load_lds_dwordx4 v[248:249], off
.LBB2_104:
	s_and_b64 vcc, exec, s[0:1]
	s_waitcnt lgkmcnt(5)
	v_mfma_f32_16x16x32_f16 v[86:89], v[182:185], v[146:149], v[86:89]
	v_mfma_f32_16x16x32_f16 v[82:85], v[178:181], v[146:149], v[82:85]
	s_waitcnt lgkmcnt(4)
	v_mfma_f32_16x16x32_f16 v[90:93], v[178:181], v[150:153], v[90:93]
	v_mfma_f32_16x16x32_f16 v[94:97], v[182:185], v[150:153], v[94:97]
	s_waitcnt lgkmcnt(2)
	v_mfma_f32_16x16x32_f16 v[106:109], v[178:181], v[236:239], v[106:109]
	v_mfma_f32_16x16x32_f16 v[110:113], v[182:185], v[236:239], v[110:113]
	v_mfma_f32_16x16x32_f16 v[98:101], v[178:181], v[232:235], v[98:101]
	v_mfma_f32_16x16x32_f16 v[102:105], v[182:185], v[232:235], v[102:105]
	ds_read_b128 v[232:235], v213 offset:12288
	ds_read_b128 v[236:239], v213 offset:14336
	s_waitcnt lgkmcnt(3)
	v_mfma_f32_16x16x32_f16 v[146:149], v[178:181], v[240:243], v[114:117]
	v_mfma_f32_16x16x32_f16 v[150:153], v[182:185], v[240:243], v[118:121]
	s_waitcnt lgkmcnt(2)
	v_mfma_f32_16x16x32_f16 v[154:157], v[178:181], v[244:247], v[122:125]
	v_mfma_f32_16x16x32_f16 v[158:161], v[182:185], v[244:247], v[126:129]
	s_waitcnt lgkmcnt(1)
	v_mfma_f32_16x16x32_f16 v[162:165], v[178:181], v[232:235], v[130:133]
	v_mfma_f32_16x16x32_f16 v[166:169], v[182:185], v[232:235], v[134:137]
	s_waitcnt lgkmcnt(0)
	v_mfma_f32_16x16x32_f16 v[170:173], v[178:181], v[236:239], v[138:141]
	v_mfma_f32_16x16x32_f16 v[174:177], v[182:185], v[236:239], v[142:145]
	s_cbranch_vccnz .LBB2_106
	ds_read_b128 v[114:117], v213 offset:16384
	s_waitcnt lgkmcnt(0)
	v_mfma_f32_16x16x32_f16 v[70:73], v[178:181], v[114:117], v[70:73]
	v_mfma_f32_16x16x32_f16 v[78:81], v[182:185], v[114:117], v[78:81]
.LBB2_106:
	s_waitcnt lgkmcnt(0)
	v_add_u32_e32 v114, s37, v199
	ds_read_b128 v[178:181], v114
	ds_read_b128 v[182:185], v114 offset:2048
	v_add_u32_e32 v213, s37, v197
	ds_read_b128 v[114:117], v213
	ds_read_b128 v[118:121], v213 offset:2048
	ds_read_b128 v[232:235], v213 offset:4096
	ds_read_b128 v[236:239], v213 offset:6144
	ds_read_b128 v[240:243], v213 offset:8192
	ds_read_b128 v[244:247], v213 offset:10240
	s_and_b64 vcc, exec, s[0:1]
	s_waitcnt lgkmcnt(5)
	v_mfma_f32_16x16x32_f16 v[134:137], v[182:185], v[114:117], v[86:89]
	v_mfma_f32_16x16x32_f16 v[138:141], v[178:181], v[114:117], v[82:85]
	s_waitcnt lgkmcnt(4)
	v_mfma_f32_16x16x32_f16 v[130:133], v[178:181], v[118:121], v[90:93]
	v_mfma_f32_16x16x32_f16 v[126:129], v[182:185], v[118:121], v[94:97]
	s_waitcnt lgkmcnt(3)
	v_mfma_f32_16x16x32_f16 v[122:125], v[178:181], v[232:235], v[98:101]
	v_mfma_f32_16x16x32_f16 v[118:121], v[182:185], v[232:235], v[102:105]
	ds_read_b128 v[232:235], v213 offset:12288
	s_waitcnt lgkmcnt(3)
	v_mfma_f32_16x16x32_f16 v[114:117], v[178:181], v[236:239], v[106:109]
	v_mfma_f32_16x16x32_f16 v[110:113], v[182:185], v[236:239], v[110:113]
	ds_read_b128 v[236:239], v213 offset:14336
	s_waitcnt lgkmcnt(3)
	v_mfma_f32_16x16x32_f16 v[106:109], v[178:181], v[240:243], v[146:149]
	v_mfma_f32_16x16x32_f16 v[102:105], v[182:185], v[240:243], v[150:153]
	s_waitcnt lgkmcnt(2)
	v_mfma_f32_16x16x32_f16 v[98:101], v[178:181], v[244:247], v[154:157]
	v_mfma_f32_16x16x32_f16 v[94:97], v[182:185], v[244:247], v[158:161]
	s_waitcnt lgkmcnt(1)
	v_mfma_f32_16x16x32_f16 v[90:93], v[178:181], v[232:235], v[162:165]
	v_mfma_f32_16x16x32_f16 v[86:89], v[182:185], v[232:235], v[166:169]
	s_waitcnt lgkmcnt(0)
	v_mfma_f32_16x16x32_f16 v[142:145], v[178:181], v[236:239], v[170:173]
	v_mfma_f32_16x16x32_f16 v[82:85], v[182:185], v[236:239], v[174:177]
	s_cbranch_vccnz .LBB2_66
	ds_read_b128 v[146:149], v213 offset:16384
	s_waitcnt lgkmcnt(0)
	v_mfma_f32_16x16x32_f16 v[70:73], v[178:181], v[146:149], v[70:73]
	v_mfma_f32_16x16x32_f16 v[78:81], v[182:185], v[146:149], v[78:81]
	s_branch .LBB2_66

	.amdhsa_kernel _Z8moe_gemmILi0EEvPKDF16_S1_PvPKyPKiPKfS1_
		.amdhsa_group_segment_fixed_size 0
		.amdhsa_private_segment_fixed_size 0
		.amdhsa_kernarg_size 56
		.amdhsa_user_sgpr_count 2
		.amdhsa_user_sgpr_dispatch_ptr 0
		.amdhsa_user_sgpr_queue_ptr 0
		.amdhsa_user_sgpr_kernarg_segment_ptr 1
		.amdhsa_user_sgpr_dispatch_id 0
		.amdhsa_user_sgpr_kernarg_preload_length 0
		.amdhsa_user_sgpr_kernarg_preload_offset 0
		.amdhsa_user_sgpr_private_segment_size 0
		.amdhsa_uses_dynamic_stack 0
		.amdhsa_enable_private_segment 0
		.amdhsa_system_sgpr_workgroup_id_x 1
		.amdhsa_system_sgpr_workgroup_id_y 0
		.amdhsa_system_sgpr_workgroup_id_z 0
		.amdhsa_system_sgpr_workgroup_info 0
		.amdhsa_system_vgpr_workitem_id 0
		.amdhsa_next_free_vgpr 252
		.amdhsa_next_free_sgpr 76
		.amdhsa_accum_offset 252
		.amdhsa_reserve_vcc 1
		.amdhsa_float_round_mode_32 0
		.amdhsa_float_round_mode_16_64 0
		.amdhsa_float_denorm_mode_32 3
		.amdhsa_float_denorm_mode_16_64 3
		.amdhsa_dx10_clamp 1
		.amdhsa_ieee_mode 1
		.amdhsa_fp16_overflow 0
		.amdhsa_tg_split 0
		.amdhsa_exception_fp_ieee_invalid_op 0
		.amdhsa_exception_fp_denorm_src 0
		.amdhsa_exception_fp_ieee_div_zero 0
		.amdhsa_exception_fp_ieee_overflow 0
		.amdhsa_exception_fp_ieee_underflow 0
		.amdhsa_exception_fp_ieee_inexact 0
		.amdhsa_exception_int_div_zero 0
	.end_amdhsa_kernel

.LBB3_92:
	s_mov_b64 s[8:9], 0x200
	v_readfirstlane_b32 s12, v110
	v_add_u32_e32 v166, 0x2000, v110
	v_lshl_add_u64 v[164:165], v[100:101], 0, s[8:9]
	s_mov_b32 m0, s12
	v_readfirstlane_b32 s12, v166
	v_add_u32_e32 v166, 0x4000, v110
	s_barrier
	s_waitcnt lgkmcnt(0)
	v_add_u32_e32 v90, s17, v115
	ds_read_b128 v[82:85], v90
	ds_read_b128 v[86:89], v90 offset:2048
	v_add_u32_e32 v125, s17, v113
	ds_read_b128 v[118:121], v125
	ds_read_b128 v[142:145], v125 offset:2048
	ds_read_b128 v[148:151], v125 offset:4096
	ds_read_b128 v[152:155], v125 offset:6144
	ds_read_b128 v[156:159], v125 offset:8192
	ds_read_b128 v[160:163], v125 offset:10240
	global_load_lds_dwordx4 v[164:165], off
	v_lshl_add_u64 v[164:165], v[98:99], 0, s[8:9]
	s_mov_b32 m0, s12
	v_readfirstlane_b32 s12, v166
	v_add_u32_e32 v166, 0x6000, v110
	global_load_lds_dwordx4 v[164:165], off
	v_lshl_add_u64 v[164:165], v[96:97], 0, s[8:9]
	s_mov_b32 m0, s12
	v_readfirstlane_b32 s12, v166
	v_add_u32_e32 v166, 0xd000, v109
	global_load_lds_dwordx4 v[164:165], off
	v_lshl_add_u64 v[164:165], v[94:95], 0, s[8:9]
	s_mov_b32 m0, s12
	v_readfirstlane_b32 s12, v166
	v_add_u32_e32 v166, 0xf000, v109
	global_load_lds_dwordx4 v[164:165], off
	v_lshl_add_u64 v[164:165], v[104:105], 0, s[8:9]
	s_mov_b32 m0, s12
	v_readfirstlane_b32 s12, v166
	global_load_lds_dwordx4 v[164:165], off
	v_lshl_add_u64 v[164:165], v[102:103], 0, s[8:9]
	s_mov_b32 m0, s12
	s_and_b64 vcc, exec, s[2:3]
	global_load_lds_dwordx4 v[164:165], off
	s_cbranch_vccnz .LBB3_94
	v_lshl_add_u64 v[164:165], v[106:107], 0, s[8:9]
	s_add_i32 s8, 0, 0x11000
	v_add_u32_e32 v166, s8, v108
	s_nop 0
	v_readfirstlane_b32 s8, v166
	s_mov_b32 m0, s8
	s_nop 0
	global_load_lds_dwordx4 v[164:165], off
.LBB3_94:
	s_and_b64 vcc, exec, s[4:5]
	s_waitcnt lgkmcnt(5)
	v_mfma_f32_16x16x32_f16 v[22:25], v[86:89], v[118:121], v[22:25]
	v_mfma_f32_16x16x32_f16 v[18:21], v[82:85], v[118:121], v[18:21]
	s_waitcnt lgkmcnt(4)
	v_mfma_f32_16x16x32_f16 v[26:29], v[82:85], v[142:145], v[26:29]
	v_mfma_f32_16x16x32_f16 v[30:33], v[86:89], v[142:145], v[30:33]
	s_waitcnt lgkmcnt(3)
	v_mfma_f32_16x16x32_f16 v[34:37], v[82:85], v[148:151], v[34:37]
	v_mfma_f32_16x16x32_f16 v[38:41], v[86:89], v[148:151], v[38:41]
	ds_read_b128 v[148:151], v125 offset:12288
	s_waitcnt lgkmcnt(3)
	v_mfma_f32_16x16x32_f16 v[42:45], v[82:85], v[152:155], v[42:45]
	v_mfma_f32_16x16x32_f16 v[46:49], v[86:89], v[152:155], v[46:49]
	ds_read_b128 v[152:155], v125 offset:14336
	s_waitcnt lgkmcnt(3)
	v_mfma_f32_16x16x32_f16 v[50:53], v[82:85], v[156:159], v[50:53]
	v_mfma_f32_16x16x32_f16 v[54:57], v[86:89], v[156:159], v[54:57]
	s_waitcnt lgkmcnt(2)
	v_mfma_f32_16x16x32_f16 v[58:61], v[82:85], v[160:163], v[58:61]
	v_mfma_f32_16x16x32_f16 v[62:65], v[86:89], v[160:163], v[62:65]
	s_waitcnt lgkmcnt(1)
	v_mfma_f32_16x16x32_f16 v[66:69], v[82:85], v[148:151], v[66:69]
	v_mfma_f32_16x16x32_f16 v[70:73], v[86:89], v[148:151], v[70:73]
	s_waitcnt lgkmcnt(0)
	v_mfma_f32_16x16x32_f16 v[74:77], v[82:85], v[152:155], v[74:77]
	v_mfma_f32_16x16x32_f16 v[78:81], v[86:89], v[152:155], v[78:81]
	s_cbranch_vccnz .LBB3_96
	ds_read_b128 v[118:121], v125 offset:16384
	s_waitcnt lgkmcnt(0)
	v_mfma_f32_16x16x32_f16 v[10:13], v[82:85], v[118:121], v[10:13]
	v_mfma_f32_16x16x32_f16 v[14:17], v[86:89], v[118:121], v[14:17]

.LBB3_98:
	s_waitcnt lgkmcnt(0)
	v_add_u32_e32 v142, s17, v116
	ds_read_b128 v[82:85], v142
	ds_read_b128 v[86:89], v142 offset:2048
	v_add_u32_e32 v141, s17, v114
	ds_read_b128 v[114:117], v141
	ds_read_b128 v[118:121], v141 offset:2048
	ds_read_b128 v[148:151], v141 offset:4096
	ds_read_b128 v[152:155], v141 offset:6144
	ds_read_b128 v[156:159], v141 offset:8192
	ds_read_b128 v[160:163], v141 offset:10240
	s_and_b64 vcc, exec, s[4:5]
	s_waitcnt lgkmcnt(5)
	v_mfma_f32_16x16x32_f16 v[22:25], v[86:89], v[114:117], v[22:25]
	v_mfma_f32_16x16x32_f16 v[18:21], v[82:85], v[114:117], v[18:21]
	s_waitcnt lgkmcnt(4)
	v_mfma_f32_16x16x32_f16 v[26:29], v[82:85], v[118:121], v[26:29]
	v_mfma_f32_16x16x32_f16 v[30:33], v[86:89], v[118:121], v[30:33]
	s_waitcnt lgkmcnt(3)
	v_mfma_f32_16x16x32_f16 v[34:37], v[82:85], v[148:151], v[34:37]
	v_mfma_f32_16x16x32_f16 v[38:41], v[86:89], v[148:151], v[38:41]
	ds_read_b128 v[148:151], v141 offset:12288
	s_waitcnt lgkmcnt(3)
	v_mfma_f32_16x16x32_f16 v[42:45], v[82:85], v[152:155], v[42:45]
	v_mfma_f32_16x16x32_f16 v[46:49], v[86:89], v[152:155], v[46:49]
	ds_read_b128 v[152:155], v141 offset:14336
	s_waitcnt lgkmcnt(3)
	v_mfma_f32_16x16x32_f16 v[50:53], v[82:85], v[156:159], v[50:53]
	v_mfma_f32_16x16x32_f16 v[54:57], v[86:89], v[156:159], v[54:57]
	s_waitcnt lgkmcnt(2)
	v_mfma_f32_16x16x32_f16 v[58:61], v[82:85], v[160:163], v[58:61]
	v_mfma_f32_16x16x32_f16 v[62:65], v[86:89], v[160:163], v[62:65]
	s_waitcnt lgkmcnt(1)
	v_mfma_f32_16x16x32_f16 v[66:69], v[82:85], v[148:151], v[66:69]
	v_mfma_f32_16x16x32_f16 v[70:73], v[86:89], v[148:151], v[70:73]
	s_waitcnt lgkmcnt(0)
	v_mfma_f32_16x16x32_f16 v[74:77], v[82:85], v[152:155], v[74:77]
	v_mfma_f32_16x16x32_f16 v[78:81], v[86:89], v[152:155], v[78:81]
	s_cbranch_vccnz .LBB3_100
	ds_read_b128 v[114:117], v141 offset:16384
	s_waitcnt lgkmcnt(0)
	v_mfma_f32_16x16x32_f16 v[10:13], v[82:85], v[114:117], v[10:13]
	v_mfma_f32_16x16x32_f16 v[14:17], v[86:89], v[114:117], v[14:17]

.LBB3_108:
	s_waitcnt lgkmcnt(0)
	ds_read_b128 v[82:85], v122 offset:20480
	ds_read_b128 v[86:89], v122 offset:22528
	ds_read_b128 v[112:115], v136
	ds_read_b128 v[116:119], v136 offset:2048
	ds_read_b128 v[148:151], v136 offset:4096
	ds_read_b128 v[152:155], v136 offset:6144
	ds_read_b128 v[156:159], v136 offset:8192
	ds_read_b128 v[160:163], v136 offset:10240
	s_and_b64 vcc, exec, s[4:5]
	s_waitcnt lgkmcnt(5)
	v_mfma_f32_16x16x32_f16 v[18:21], v[82:85], v[112:115], v[18:21]
	v_mfma_f32_16x16x32_f16 v[22:25], v[86:89], v[112:115], v[22:25]
	s_waitcnt lgkmcnt(4)
	v_mfma_f32_16x16x32_f16 v[26:29], v[82:85], v[116:119], v[26:29]
	v_mfma_f32_16x16x32_f16 v[30:33], v[86:89], v[116:119], v[30:33]
	s_waitcnt lgkmcnt(3)
	v_mfma_f32_16x16x32_f16 v[34:37], v[82:85], v[148:151], v[34:37]
	v_mfma_f32_16x16x32_f16 v[38:41], v[86:89], v[148:151], v[38:41]
	ds_read_b128 v[148:151], v136 offset:12288
	s_waitcnt lgkmcnt(3)
	v_mfma_f32_16x16x32_f16 v[42:45], v[82:85], v[152:155], v[42:45]
	v_mfma_f32_16x16x32_f16 v[46:49], v[86:89], v[152:155], v[46:49]
	ds_read_b128 v[152:155], v136 offset:14336
	s_waitcnt lgkmcnt(3)
	v_mfma_f32_16x16x32_f16 v[50:53], v[82:85], v[156:159], v[50:53]
	v_mfma_f32_16x16x32_f16 v[54:57], v[86:89], v[156:159], v[54:57]
	s_waitcnt lgkmcnt(2)
	v_mfma_f32_16x16x32_f16 v[58:61], v[82:85], v[160:163], v[58:61]
	v_mfma_f32_16x16x32_f16 v[62:65], v[86:89], v[160:163], v[62:65]
	s_waitcnt lgkmcnt(1)
	v_mfma_f32_16x16x32_f16 v[66:69], v[82:85], v[148:151], v[66:69]
	v_mfma_f32_16x16x32_f16 v[70:73], v[86:89], v[148:151], v[70:73]
	s_waitcnt lgkmcnt(0)
	v_mfma_f32_16x16x32_f16 v[74:77], v[82:85], v[152:155], v[74:77]
	v_mfma_f32_16x16x32_f16 v[78:81], v[86:89], v[152:155], v[78:81]
	s_cbranch_vccnz .LBB3_110
	ds_read_b128 v[112:115], v136 offset:16384
	s_waitcnt lgkmcnt(0)
	v_mfma_f32_16x16x32_f16 v[10:13], v[82:85], v[112:115], v[10:13]
	v_mfma_f32_16x16x32_f16 v[14:17], v[86:89], v[112:115], v[14:17]

.LBB3_112:
	s_waitcnt lgkmcnt(0)
	ds_read_b128 v[82:85], v123 offset:20480
	ds_read_b128 v[86:89], v123 offset:22528
	ds_read_b128 v[112:115], v137
	ds_read_b128 v[116:119], v137 offset:2048
	ds_read_b128 v[148:151], v137 offset:4096
	ds_read_b128 v[152:155], v137 offset:6144
	ds_read_b128 v[156:159], v137 offset:8192
	ds_read_b128 v[160:163], v137 offset:10240
	s_and_b64 vcc, exec, s[4:5]
	s_waitcnt lgkmcnt(5)
	v_mfma_f32_16x16x32_f16 v[18:21], v[82:85], v[112:115], v[18:21]
	v_mfma_f32_16x16x32_f16 v[22:25], v[86:89], v[112:115], v[22:25]
	s_waitcnt lgkmcnt(4)
	v_mfma_f32_16x16x32_f16 v[26:29], v[82:85], v[116:119], v[26:29]
	v_mfma_f32_16x16x32_f16 v[30:33], v[86:89], v[116:119], v[30:33]
	s_waitcnt lgkmcnt(3)
	v_mfma_f32_16x16x32_f16 v[34:37], v[82:85], v[148:151], v[34:37]
	v_mfma_f32_16x16x32_f16 v[38:41], v[86:89], v[148:151], v[38:41]
	ds_read_b128 v[148:151], v137 offset:12288
	s_waitcnt lgkmcnt(3)
	v_mfma_f32_16x16x32_f16 v[42:45], v[82:85], v[152:155], v[42:45]
	v_mfma_f32_16x16x32_f16 v[46:49], v[86:89], v[152:155], v[46:49]
	ds_read_b128 v[152:155], v137 offset:14336
	s_waitcnt lgkmcnt(3)
	v_mfma_f32_16x16x32_f16 v[50:53], v[82:85], v[156:159], v[50:53]
	v_mfma_f32_16x16x32_f16 v[54:57], v[86:89], v[156:159], v[54:57]
	s_waitcnt lgkmcnt(2)
	v_mfma_f32_16x16x32_f16 v[58:61], v[82:85], v[160:163], v[58:61]
	v_mfma_f32_16x16x32_f16 v[62:65], v[86:89], v[160:163], v[62:65]
	s_waitcnt lgkmcnt(1)
	v_mfma_f32_16x16x32_f16 v[66:69], v[82:85], v[148:151], v[66:69]
	v_mfma_f32_16x16x32_f16 v[70:73], v[86:89], v[148:151], v[70:73]
	s_waitcnt lgkmcnt(0)
	v_mfma_f32_16x16x32_f16 v[74:77], v[82:85], v[152:155], v[74:77]
	v_mfma_f32_16x16x32_f16 v[78:81], v[86:89], v[152:155], v[78:81]
	s_cbranch_vccz .LBB3_182
	s_and_b64 vcc, exec, s[6:7]
	s_cbranch_vccz .LBB3_183

.LBB3_117:
	v_add_u32_e32 v166, 0x5000, v109
	s_mov_b64 s[10:11], 0x300
	v_readfirstlane_b32 s12, v166
	v_add_u32_e32 v166, 0x7000, v109
	v_lshl_add_u64 v[164:165], v[100:101], 0, s[10:11]
	s_mov_b32 m0, s12
	v_readfirstlane_b32 s12, v166
	v_add_u32_e32 v166, 0x9000, v109
	s_barrier
	s_waitcnt lgkmcnt(0)
	ds_read_b128 v[82:85], v124 offset:53248
	ds_read_b128 v[86:89], v124 offset:55296
	ds_read_b128 v[112:115], v136 offset:53248
	ds_read_b128 v[116:119], v136 offset:55296
	ds_read_b128 v[148:151], v136 offset:57344
	ds_read_b128 v[152:155], v136 offset:59392
	ds_read_b128 v[156:159], v136 offset:61440
	ds_read_b128 v[160:163], v136 offset:63488
	global_load_lds_dwordx4 v[164:165], off
	v_lshl_add_u64 v[164:165], v[98:99], 0, s[10:11]
	s_mov_b32 m0, s12
	v_readfirstlane_b32 s12, v166
	v_add_u32_e32 v166, 0xb000, v109
	global_load_lds_dwordx4 v[164:165], off
	v_lshl_add_u64 v[164:165], v[96:97], 0, s[10:11]
	s_mov_b32 m0, s12
	v_readfirstlane_b32 s12, v166
	global_load_lds_dwordx4 v[164:165], off
	v_lshl_add_u64 v[164:165], v[94:95], 0, s[10:11]
	s_mov_b32 m0, s12
	v_readfirstlane_b32 s12, v109
	v_add_u32_e32 v166, 0x2000, v109
	global_load_lds_dwordx4 v[164:165], off
	v_lshl_add_u64 v[164:165], v[104:105], 0, s[10:11]
	s_mov_b32 m0, s12
	v_readfirstlane_b32 s12, v166
	global_load_lds_dwordx4 v[164:165], off
	v_lshl_add_u64 v[164:165], v[102:103], 0, s[10:11]
	s_mov_b32 m0, s12
	s_and_b64 vcc, exec, s[2:3]
	global_load_lds_dwordx4 v[164:165], off
	s_cbranch_vccnz .LBB3_119
	v_add_u32_e32 v166, 0x4000, v109
	v_lshl_add_u64 v[164:165], v[106:107], 0, s[10:11]
	v_readfirstlane_b32 s10, v166
	s_mov_b32 m0, s10
	s_nop 0
	global_load_lds_dwordx4 v[164:165], off
.LBB3_119:
	s_and_b64 vcc, exec, s[4:5]
	s_waitcnt lgkmcnt(5)
	v_mfma_f32_16x16x32_f16 v[18:21], v[82:85], v[112:115], v[18:21]
	v_mfma_f32_16x16x32_f16 v[22:25], v[86:89], v[112:115], v[22:25]
	s_waitcnt lgkmcnt(4)
	v_mfma_f32_16x16x32_f16 v[26:29], v[82:85], v[116:119], v[26:29]
	v_mfma_f32_16x16x32_f16 v[30:33], v[86:89], v[116:119], v[30:33]
	s_waitcnt lgkmcnt(3)
	v_mfma_f32_16x16x32_f16 v[34:37], v[82:85], v[148:151], v[34:37]
	v_mfma_f32_16x16x32_f16 v[38:41], v[86:89], v[148:151], v[38:41]
	ds_read_b128 v[148:151], v138 offset:12288
	s_waitcnt lgkmcnt(3)
	v_mfma_f32_16x16x32_f16 v[42:45], v[82:85], v[152:155], v[42:45]
	v_mfma_f32_16x16x32_f16 v[46:49], v[86:89], v[152:155], v[46:49]
	ds_read_b128 v[152:155], v138 offset:14336
	s_waitcnt lgkmcnt(3)
	v_mfma_f32_16x16x32_f16 v[50:53], v[82:85], v[156:159], v[50:53]
	v_mfma_f32_16x16x32_f16 v[54:57], v[86:89], v[156:159], v[54:57]
	s_waitcnt lgkmcnt(2)
	v_mfma_f32_16x16x32_f16 v[58:61], v[82:85], v[160:163], v[58:61]
	v_mfma_f32_16x16x32_f16 v[62:65], v[86:89], v[160:163], v[62:65]
	s_waitcnt lgkmcnt(1)
	v_mfma_f32_16x16x32_f16 v[66:69], v[82:85], v[148:151], v[66:69]
	v_mfma_f32_16x16x32_f16 v[70:73], v[86:89], v[148:151], v[70:73]
	s_waitcnt lgkmcnt(0)
	v_mfma_f32_16x16x32_f16 v[74:77], v[82:85], v[152:155], v[74:77]
	v_mfma_f32_16x16x32_f16 v[78:81], v[86:89], v[152:155], v[78:81]
	s_cbranch_vccnz .LBB3_121
	ds_read_b128 v[112:115], v138 offset:16384
	s_waitcnt lgkmcnt(0)
	v_mfma_f32_16x16x32_f16 v[10:13], v[82:85], v[112:115], v[10:13]
	v_mfma_f32_16x16x32_f16 v[14:17], v[86:89], v[112:115], v[14:17]

.LBB3_123:
	s_waitcnt lgkmcnt(0)
	ds_read_b128 v[82:85], v140 offset:53248
	ds_read_b128 v[86:89], v140 offset:55296
	ds_read_b128 v[112:115], v137 offset:53248
	ds_read_b128 v[116:119], v137 offset:55296
	ds_read_b128 v[148:151], v137 offset:57344
	ds_read_b128 v[152:155], v137 offset:59392
	ds_read_b128 v[156:159], v137 offset:61440
	ds_read_b128 v[160:163], v137 offset:63488
	s_and_b64 vcc, exec, s[4:5]
	s_waitcnt lgkmcnt(5)
	v_mfma_f32_16x16x32_f16 v[18:21], v[82:85], v[112:115], v[18:21]
	v_mfma_f32_16x16x32_f16 v[22:25], v[86:89], v[112:115], v[22:25]
	s_waitcnt lgkmcnt(4)
	v_mfma_f32_16x16x32_f16 v[26:29], v[82:85], v[116:119], v[26:29]
	v_mfma_f32_16x16x32_f16 v[30:33], v[86:89], v[116:119], v[30:33]
	s_waitcnt lgkmcnt(3)
	v_mfma_f32_16x16x32_f16 v[34:37], v[82:85], v[148:151], v[34:37]
	v_mfma_f32_16x16x32_f16 v[38:41], v[86:89], v[148:151], v[38:41]
	ds_read_b128 v[148:151], v139 offset:12288
	s_waitcnt lgkmcnt(3)
	v_mfma_f32_16x16x32_f16 v[42:45], v[82:85], v[152:155], v[42:45]
	v_mfma_f32_16x16x32_f16 v[46:49], v[86:89], v[152:155], v[46:49]
	ds_read_b128 v[152:155], v139 offset:14336
	s_waitcnt lgkmcnt(3)
	v_mfma_f32_16x16x32_f16 v[50:53], v[82:85], v[156:159], v[50:53]
	v_mfma_f32_16x16x32_f16 v[54:57], v[86:89], v[156:159], v[54:57]
	s_waitcnt lgkmcnt(2)
	v_mfma_f32_16x16x32_f16 v[58:61], v[82:85], v[160:163], v[58:61]
	v_mfma_f32_16x16x32_f16 v[62:65], v[86:89], v[160:163], v[62:65]
	s_waitcnt lgkmcnt(1)
	v_mfma_f32_16x16x32_f16 v[66:69], v[82:85], v[148:151], v[66:69]
	v_mfma_f32_16x16x32_f16 v[70:73], v[86:89], v[148:151], v[70:73]
	s_waitcnt lgkmcnt(0)
	v_mfma_f32_16x16x32_f16 v[74:77], v[82:85], v[152:155], v[74:77]
	v_mfma_f32_16x16x32_f16 v[78:81], v[86:89], v[152:155], v[78:81]
	s_cbranch_vccz .LBB3_185
	s_and_b64 vcc, exec, s[6:7]
	s_cbranch_vccz .LBB3_186

.LBB3_128:
	s_mov_b64 s[10:11], 0x380
	v_readfirstlane_b32 s12, v110
	v_add_u32_e32 v166, 0x2000, v110
	v_lshl_add_u64 v[164:165], v[100:101], 0, s[10:11]
	s_mov_b32 m0, s12
	v_readfirstlane_b32 s12, v166
	v_add_u32_e32 v166, 0x4000, v110
	s_barrier
	s_waitcnt lgkmcnt(0)
	ds_read_b128 v[114:117], v90
	ds_read_b128 v[118:121], v90 offset:2048
	ds_read_b128 v[82:85], v125
	ds_read_b128 v[86:89], v125 offset:2048
	ds_read_b128 v[148:151], v125 offset:4096
	ds_read_b128 v[152:155], v125 offset:6144
	ds_read_b128 v[156:159], v125 offset:8192
	ds_read_b128 v[160:163], v125 offset:10240
	global_load_lds_dwordx4 v[164:165], off
	v_lshl_add_u64 v[164:165], v[98:99], 0, s[10:11]
	s_mov_b32 m0, s12
	v_readfirstlane_b32 s12, v166
	v_add_u32_e32 v166, 0x6000, v110
	global_load_lds_dwordx4 v[164:165], off
	v_lshl_add_u64 v[164:165], v[96:97], 0, s[10:11]
	s_mov_b32 m0, s12
	v_readfirstlane_b32 s12, v166
	v_add_u32_e32 v166, 0xd000, v109
	global_load_lds_dwordx4 v[164:165], off
	v_lshl_add_u64 v[164:165], v[94:95], 0, s[10:11]
	s_mov_b32 m0, s12
	v_readfirstlane_b32 s12, v166
	v_add_u32_e32 v166, 0xf000, v109
	global_load_lds_dwordx4 v[164:165], off
	v_lshl_add_u64 v[164:165], v[104:105], 0, s[10:11]
	s_mov_b32 m0, s12
	v_readfirstlane_b32 s12, v166
	global_load_lds_dwordx4 v[164:165], off
	v_lshl_add_u64 v[164:165], v[102:103], 0, s[10:11]
	s_mov_b32 m0, s12
	s_and_b64 vcc, exec, s[2:3]
	global_load_lds_dwordx4 v[164:165], off
	s_cbranch_vccnz .LBB3_130
	s_add_i32 s2, 0, 0x11000
	v_add_u32_e32 v166, s2, v108
	v_lshl_add_u64 v[164:165], v[106:107], 0, s[10:11]
	v_readfirstlane_b32 s2, v166
	s_mov_b32 m0, s2
	s_nop 0
	global_load_lds_dwordx4 v[164:165], off
.LBB3_130:
	s_and_b64 vcc, exec, s[4:5]
	s_waitcnt lgkmcnt(5)
	v_mfma_f32_16x16x32_f16 v[18:21], v[114:117], v[82:85], v[18:21]
	v_mfma_f32_16x16x32_f16 v[22:25], v[118:121], v[82:85], v[22:25]
	s_waitcnt lgkmcnt(4)
	v_mfma_f32_16x16x32_f16 v[26:29], v[114:117], v[86:89], v[26:29]
	v_mfma_f32_16x16x32_f16 v[30:33], v[118:121], v[86:89], v[30:33]
	s_waitcnt lgkmcnt(2)
	v_mfma_f32_16x16x32_f16 v[42:45], v[114:117], v[152:155], v[42:45]
	v_mfma_f32_16x16x32_f16 v[46:49], v[118:121], v[152:155], v[46:49]
	v_mfma_f32_16x16x32_f16 v[34:37], v[114:117], v[148:151], v[34:37]
	v_mfma_f32_16x16x32_f16 v[38:41], v[118:121], v[148:151], v[38:41]
	ds_read_b128 v[148:151], v125 offset:12288
	ds_read_b128 v[152:155], v125 offset:14336
	s_waitcnt lgkmcnt(3)
	v_mfma_f32_16x16x32_f16 v[82:85], v[114:117], v[156:159], v[50:53]
	v_mfma_f32_16x16x32_f16 v[86:89], v[118:121], v[156:159], v[54:57]
	s_nop 1
	s_waitcnt lgkmcnt(2)
	v_mfma_f32_16x16x32_f16 v[90:93], v[114:117], v[160:163], v[58:61]
	v_mfma_f32_16x16x32_f16 v[94:97], v[118:121], v[160:163], v[62:65]
	s_waitcnt lgkmcnt(1)
	v_mfma_f32_16x16x32_f16 v[98:101], v[114:117], v[148:151], v[66:69]
	v_mfma_f32_16x16x32_f16 v[102:105], v[118:121], v[148:151], v[70:73]
	s_waitcnt lgkmcnt(0)
	v_mfma_f32_16x16x32_f16 v[106:109], v[114:117], v[152:155], v[74:77]
	v_mfma_f32_16x16x32_f16 v[110:113], v[118:121], v[152:155], v[78:81]
	s_cbranch_vccnz .LBB3_132
	ds_read_b128 v[50:53], v125 offset:16384
	s_waitcnt lgkmcnt(0)
	v_mfma_f32_16x16x32_f16 v[10:13], v[114:117], v[50:53], v[10:13]
	v_mfma_f32_16x16x32_f16 v[14:17], v[118:121], v[50:53], v[14:17]

.LBB3_134:
	s_waitcnt lgkmcnt(0)
	ds_read_b128 v[114:117], v142
	ds_read_b128 v[118:121], v142 offset:2048
	ds_read_b128 v[54:57], v141
	ds_read_b128 v[58:61], v141 offset:2048
	ds_read_b128 v[148:151], v141 offset:4096
	ds_read_b128 v[152:155], v141 offset:6144
	ds_read_b128 v[156:159], v141 offset:8192
	ds_read_b128 v[160:163], v141 offset:10240
	s_and_b64 vcc, exec, s[4:5]
	s_waitcnt lgkmcnt(5)
	v_mfma_f32_16x16x32_f16 v[50:53], v[114:117], v[54:57], v[18:21]
	v_mfma_f32_16x16x32_f16 v[54:57], v[118:121], v[54:57], v[22:25]
	s_waitcnt lgkmcnt(4)
	v_mfma_f32_16x16x32_f16 v[18:21], v[114:117], v[58:61], v[26:29]
	v_mfma_f32_16x16x32_f16 v[22:25], v[118:121], v[58:61], v[30:33]
	s_nop 1
	s_waitcnt lgkmcnt(3)
	v_mfma_f32_16x16x32_f16 v[58:61], v[114:117], v[148:151], v[34:37]
	v_mfma_f32_16x16x32_f16 v[62:65], v[118:121], v[148:151], v[38:41]
	ds_read_b128 v[148:151], v141 offset:12288
	s_nop 1
	s_waitcnt lgkmcnt(3)
	v_mfma_f32_16x16x32_f16 v[26:29], v[114:117], v[152:155], v[42:45]
	v_mfma_f32_16x16x32_f16 v[30:33], v[118:121], v[152:155], v[46:49]
	ds_read_b128 v[152:155], v141 offset:14336
	s_nop 1
	s_waitcnt lgkmcnt(3)
	v_mfma_f32_16x16x32_f16 v[66:69], v[114:117], v[156:159], v[82:85]
	v_mfma_f32_16x16x32_f16 v[70:73], v[118:121], v[156:159], v[86:89]
	s_waitcnt lgkmcnt(2)
	v_mfma_f32_16x16x32_f16 v[34:37], v[114:117], v[160:163], v[90:93]
	v_mfma_f32_16x16x32_f16 v[38:41], v[118:121], v[160:163], v[94:97]
	s_waitcnt lgkmcnt(1)
	v_mfma_f32_16x16x32_f16 v[74:77], v[114:117], v[148:151], v[98:101]
	v_mfma_f32_16x16x32_f16 v[78:81], v[118:121], v[148:151], v[102:105]
	s_waitcnt lgkmcnt(0)
	v_mfma_f32_16x16x32_f16 v[42:45], v[114:117], v[152:155], v[106:109]
	v_mfma_f32_16x16x32_f16 v[46:49], v[118:121], v[152:155], v[110:113]
	s_cbranch_vccz .LBB3_188
	s_and_b64 vcc, exec, s[6:7]
	s_cbranch_vccz .LBB3_189

.LBB3_139:
	s_barrier
	s_waitcnt lgkmcnt(0)
	ds_read_b128 v[82:85], v122 offset:20480
	ds_read_b128 v[86:89], v122 offset:22528
	ds_read_b128 v[90:93], v136
	s_and_b64 vcc, exec, s[4:5]
	s_waitcnt lgkmcnt(0)
	v_mfma_f32_16x16x32_f16 v[50:53], v[82:85], v[90:93], v[50:53]
	v_mfma_f32_16x16x32_f16 v[54:57], v[86:89], v[90:93], v[54:57]
	ds_read_b128 v[90:93], v136 offset:2048
	ds_read_b128 v[148:151], v136 offset:4096
	ds_read_b128 v[152:155], v136 offset:6144
	ds_read_b128 v[156:159], v136 offset:8192
	ds_read_b128 v[160:163], v136 offset:10240
	s_waitcnt lgkmcnt(4)
	v_mfma_f32_16x16x32_f16 v[18:21], v[82:85], v[90:93], v[18:21]
	v_mfma_f32_16x16x32_f16 v[22:25], v[86:89], v[90:93], v[22:25]
	s_waitcnt lgkmcnt(3)
	v_mfma_f32_16x16x32_f16 v[58:61], v[82:85], v[148:151], v[58:61]
	v_mfma_f32_16x16x32_f16 v[62:65], v[86:89], v[148:151], v[62:65]
	ds_read_b128 v[148:151], v136 offset:12288
	s_waitcnt lgkmcnt(3)
	v_mfma_f32_16x16x32_f16 v[26:29], v[82:85], v[152:155], v[26:29]
	v_mfma_f32_16x16x32_f16 v[30:33], v[86:89], v[152:155], v[30:33]
	ds_read_b128 v[152:155], v136 offset:14336
	s_waitcnt lgkmcnt(3)
	v_mfma_f32_16x16x32_f16 v[66:69], v[82:85], v[156:159], v[66:69]
	v_mfma_f32_16x16x32_f16 v[70:73], v[86:89], v[156:159], v[70:73]
	s_waitcnt lgkmcnt(2)
	v_mfma_f32_16x16x32_f16 v[34:37], v[82:85], v[160:163], v[34:37]
	v_mfma_f32_16x16x32_f16 v[38:41], v[86:89], v[160:163], v[38:41]
	s_waitcnt lgkmcnt(1)
	v_mfma_f32_16x16x32_f16 v[74:77], v[82:85], v[148:151], v[74:77]
	v_mfma_f32_16x16x32_f16 v[78:81], v[86:89], v[148:151], v[78:81]
	s_waitcnt lgkmcnt(0)
	v_mfma_f32_16x16x32_f16 v[42:45], v[82:85], v[152:155], v[42:45]
	v_mfma_f32_16x16x32_f16 v[46:49], v[86:89], v[152:155], v[46:49]
	s_cbranch_vccnz .LBB3_141
	ds_read_b128 v[90:93], v136 offset:16384
	s_waitcnt lgkmcnt(0)
	v_mfma_f32_16x16x32_f16 v[10:13], v[82:85], v[90:93], v[10:13]
	v_mfma_f32_16x16x32_f16 v[14:17], v[86:89], v[90:93], v[14:17]

.LBB3_143:
	s_waitcnt lgkmcnt(0)
	ds_read_b128 v[82:85], v123 offset:20480
	ds_read_b128 v[86:89], v123 offset:22528
	ds_read_b128 v[90:93], v137
	ds_read_b128 v[94:97], v137 offset:2048
	ds_read_b128 v[148:151], v137 offset:4096
	ds_read_b128 v[152:155], v137 offset:6144
	ds_read_b128 v[156:159], v137 offset:8192
	ds_read_b128 v[160:163], v137 offset:10240
	s_and_b64 vcc, exec, s[4:5]
	s_waitcnt lgkmcnt(5)
	v_mfma_f32_16x16x32_f16 v[50:53], v[82:85], v[90:93], v[50:53]
	v_mfma_f32_16x16x32_f16 v[54:57], v[86:89], v[90:93], v[54:57]
	s_waitcnt lgkmcnt(4)
	v_mfma_f32_16x16x32_f16 v[18:21], v[82:85], v[94:97], v[18:21]
	v_mfma_f32_16x16x32_f16 v[22:25], v[86:89], v[94:97], v[22:25]
	s_waitcnt lgkmcnt(3)
	v_mfma_f32_16x16x32_f16 v[58:61], v[82:85], v[148:151], v[58:61]
	v_mfma_f32_16x16x32_f16 v[62:65], v[86:89], v[148:151], v[62:65]
	ds_read_b128 v[148:151], v137 offset:12288
	s_waitcnt lgkmcnt(3)
	v_mfma_f32_16x16x32_f16 v[26:29], v[82:85], v[152:155], v[26:29]
	v_mfma_f32_16x16x32_f16 v[30:33], v[86:89], v[152:155], v[30:33]
	ds_read_b128 v[152:155], v137 offset:14336
	s_waitcnt lgkmcnt(3)
	v_mfma_f32_16x16x32_f16 v[66:69], v[82:85], v[156:159], v[66:69]
	v_mfma_f32_16x16x32_f16 v[70:73], v[86:89], v[156:159], v[70:73]
	s_waitcnt lgkmcnt(2)
	v_mfma_f32_16x16x32_f16 v[34:37], v[82:85], v[160:163], v[34:37]
	v_mfma_f32_16x16x32_f16 v[38:41], v[86:89], v[160:163], v[38:41]
	s_waitcnt lgkmcnt(1)
	v_mfma_f32_16x16x32_f16 v[74:77], v[82:85], v[148:151], v[74:77]
	v_mfma_f32_16x16x32_f16 v[78:81], v[86:89], v[148:151], v[78:81]
	s_waitcnt lgkmcnt(0)
	v_mfma_f32_16x16x32_f16 v[42:45], v[82:85], v[152:155], v[42:45]
	v_mfma_f32_16x16x32_f16 v[46:49], v[86:89], v[152:155], v[46:49]
	s_cbranch_vccnz .LBB3_145
	ds_read_b128 v[90:93], v137 offset:16384
	s_waitcnt lgkmcnt(0)
	v_mfma_f32_16x16x32_f16 v[10:13], v[82:85], v[90:93], v[10:13]
	v_mfma_f32_16x16x32_f16 v[14:17], v[86:89], v[90:93], v[14:17]

.LBB3_147:
	s_waitcnt vmcnt(0)
	s_barrier
	s_waitcnt lgkmcnt(0)
	ds_read_b128 v[118:121], v124 offset:53248
	ds_read_b128 v[122:125], v124 offset:55296
	ds_read_b128 v[82:85], v136 offset:53248
	s_and_b64 vcc, exec, s[4:5]
	s_waitcnt lgkmcnt(0)
	v_mfma_f32_16x16x32_f16 v[50:53], v[118:121], v[82:85], v[50:53]
	v_mfma_f32_16x16x32_f16 v[54:57], v[122:125], v[82:85], v[54:57]
	ds_read_b128 v[82:85], v136 offset:55296
	ds_read_b128 v[148:151], v136 offset:57344
	ds_read_b128 v[152:155], v136 offset:59392
	ds_read_b128 v[156:159], v136 offset:63488
	ds_read_b128 v[160:163], v136 offset:61440
	s_waitcnt lgkmcnt(4)
	v_mfma_f32_16x16x32_f16 v[98:101], v[122:125], v[82:85], v[22:25]
	s_nop 2
	v_mfma_f32_16x16x32_f16 v[94:97], v[118:121], v[82:85], v[18:21]
	s_waitcnt lgkmcnt(3)
	v_mfma_f32_16x16x32_f16 v[18:21], v[118:121], v[148:151], v[58:61]
	s_nop 2
	s_waitcnt lgkmcnt(2)
	v_mfma_f32_16x16x32_f16 v[102:105], v[118:121], v[152:155], v[26:29]
	v_mfma_f32_16x16x32_f16 v[106:109], v[122:125], v[152:155], v[30:33]
	ds_read_b128 v[152:155], v138 offset:12288
	s_nop 1
	s_waitcnt lgkmcnt(2)
	v_mfma_f32_16x16x32_f16 v[110:113], v[122:125], v[156:159], v[38:41]
	s_nop 2
	s_waitcnt lgkmcnt(0)
	v_mfma_f32_16x16x32_f16 v[82:85], v[118:121], v[152:155], v[74:77]
	v_mfma_f32_16x16x32_f16 v[86:89], v[122:125], v[152:155], v[78:81]
	ds_read_b128 v[152:155], v138 offset:14336
	v_mfma_f32_16x16x32_f16 v[22:25], v[122:125], v[148:151], v[62:65]
	v_mfma_f32_16x16x32_f16 v[26:29], v[118:121], v[160:163], v[66:69]
	v_mfma_f32_16x16x32_f16 v[30:33], v[122:125], v[160:163], v[70:73]
	v_mfma_f32_16x16x32_f16 v[34:37], v[118:121], v[156:159], v[34:37]
	s_waitcnt lgkmcnt(0)
	v_mfma_f32_16x16x32_f16 v[114:117], v[118:121], v[152:155], v[42:45]
	v_mfma_f32_16x16x32_f16 v[90:93], v[122:125], v[152:155], v[46:49]
	s_cbranch_vccnz .LBB3_149
	ds_read_b128 v[38:41], v138 offset:16384
	s_waitcnt lgkmcnt(0)
	v_mfma_f32_16x16x32_f16 v[10:13], v[118:121], v[38:41], v[10:13]
	v_mfma_f32_16x16x32_f16 v[14:17], v[122:125], v[38:41], v[14:17]

	.amdhsa_kernel _Z8moe_gemmILi1EEvPKDF16_S1_PvPKyPKiPKfS1_
		.amdhsa_group_segment_fixed_size 0
		.amdhsa_private_segment_fixed_size 0
		.amdhsa_kernarg_size 56
		.amdhsa_user_sgpr_count 2
		.amdhsa_user_sgpr_dispatch_ptr 0
		.amdhsa_user_sgpr_queue_ptr 0
		.amdhsa_user_sgpr_kernarg_segment_ptr 1
		.amdhsa_user_sgpr_dispatch_id 0
		.amdhsa_user_sgpr_kernarg_preload_length 0
		.amdhsa_user_sgpr_kernarg_preload_offset 0
		.amdhsa_user_sgpr_private_segment_size 0
		.amdhsa_uses_dynamic_stack 0
		.amdhsa_enable_private_segment 0
		.amdhsa_system_sgpr_workgroup_id_x 1
		.amdhsa_system_sgpr_workgroup_id_y 0
		.amdhsa_system_sgpr_workgroup_id_z 0
		.amdhsa_system_sgpr_workgroup_info 0
		.amdhsa_system_vgpr_workitem_id 0
		.amdhsa_next_free_vgpr 168
		.amdhsa_next_free_sgpr 62
		.amdhsa_accum_offset 168
		.amdhsa_reserve_vcc 1
		.amdhsa_float_round_mode_32 0
		.amdhsa_float_round_mode_16_64 0
		.amdhsa_float_denorm_mode_32 3
		.amdhsa_float_denorm_mode_16_64 3
		.amdhsa_dx10_clamp 1
		.amdhsa_ieee_mode 1
		.amdhsa_fp16_overflow 0
		.amdhsa_tg_split 0
		.amdhsa_exception_fp_ieee_invalid_op 0
		.amdhsa_exception_fp_denorm_src 0
		.amdhsa_exception_fp_ieee_div_zero 0
		.amdhsa_exception_fp_ieee_overflow 0
		.amdhsa_exception_fp_ieee_underflow 0
		.amdhsa_exception_fp_ieee_inexact 0
		.amdhsa_exception_int_div_zero 0
	.end_amdhsa_kernel

.LBB4_107:
	s_mov_b64 s[28:29], 0x200
	v_readfirstlane_b32 s34, v136
	v_add_u32_e32 v174, 0x2000, v136
	v_lshl_add_u64 v[172:173], v[116:117], 0, s[28:29]
	s_mov_b32 m0, s34
	v_readfirstlane_b32 s34, v174
	v_add_u32_e32 v174, 0x4000, v136
	s_barrier
	s_waitcnt lgkmcnt(0)
	v_add_u32_e32 v90, s35, v106
	ds_read_b128 v[82:85], v90
	ds_read_b128 v[86:89], v90 offset:2048
	v_add_u32_e32 v146, s35, v146
	ds_read_b128 v[92:95], v146
	ds_read_b128 v[96:99], v146 offset:2048
	ds_read_b128 v[156:159], v146 offset:4096
	ds_read_b128 v[160:163], v146 offset:6144
	ds_read_b128 v[164:167], v146 offset:8192
	ds_read_b128 v[168:171], v146 offset:10240
	global_load_lds_dwordx4 v[172:173], off
	v_lshl_add_u64 v[172:173], v[114:115], 0, s[28:29]
	s_mov_b32 m0, s34
	v_readfirstlane_b32 s34, v174
	v_add_u32_e32 v174, 0x6000, v136
	global_load_lds_dwordx4 v[172:173], off
	v_lshl_add_u64 v[172:173], v[112:113], 0, s[28:29]
	s_mov_b32 m0, s34
	v_readfirstlane_b32 s34, v174
	v_add_u32_e32 v174, 0xd000, v135
	global_load_lds_dwordx4 v[172:173], off
	v_lshl_add_u64 v[172:173], v[110:111], 0, s[28:29]
	s_mov_b32 m0, s34
	v_readfirstlane_b32 s34, v174
	v_add_u32_e32 v174, 0xf000, v135
	global_load_lds_dwordx4 v[172:173], off
	v_lshl_add_u64 v[172:173], v[120:121], 0, s[28:29]
	s_mov_b32 m0, s34
	v_readfirstlane_b32 s34, v174
	global_load_lds_dwordx4 v[172:173], off
	v_lshl_add_u64 v[172:173], v[118:119], 0, s[28:29]
	s_mov_b32 m0, s34
	s_and_b64 vcc, exec, s[14:15]
	global_load_lds_dwordx4 v[172:173], off
	s_cbranch_vccnz .LBB4_109
	v_lshl_add_u64 v[172:173], v[122:123], 0, s[28:29]
	s_add_i32 s28, 0, 0x11000
	v_add_u32_e32 v174, s28, v1
	s_nop 0
	v_readfirstlane_b32 s28, v174
	s_mov_b32 m0, s28
	s_nop 0
	global_load_lds_dwordx4 v[172:173], off
.LBB4_109:
	s_and_b64 vcc, exec, s[24:25]
	s_waitcnt lgkmcnt(5)
	v_mfma_f32_16x16x32_f16 v[22:25], v[86:89], v[92:95], v[22:25]
	v_mfma_f32_16x16x32_f16 v[18:21], v[82:85], v[92:95], v[18:21]
	s_waitcnt lgkmcnt(4)
	v_mfma_f32_16x16x32_f16 v[26:29], v[82:85], v[96:99], v[26:29]
	v_mfma_f32_16x16x32_f16 v[30:33], v[86:89], v[96:99], v[30:33]
	s_waitcnt lgkmcnt(3)
	v_mfma_f32_16x16x32_f16 v[34:37], v[82:85], v[156:159], v[34:37]
	v_mfma_f32_16x16x32_f16 v[38:41], v[86:89], v[156:159], v[38:41]
	ds_read_b128 v[156:159], v146 offset:12288
	s_waitcnt lgkmcnt(3)
	v_mfma_f32_16x16x32_f16 v[42:45], v[82:85], v[160:163], v[42:45]
	v_mfma_f32_16x16x32_f16 v[46:49], v[86:89], v[160:163], v[46:49]
	ds_read_b128 v[160:163], v146 offset:14336
	s_waitcnt lgkmcnt(3)
	v_mfma_f32_16x16x32_f16 v[50:53], v[82:85], v[164:167], v[50:53]
	v_mfma_f32_16x16x32_f16 v[54:57], v[86:89], v[164:167], v[54:57]
	s_waitcnt lgkmcnt(2)
	v_mfma_f32_16x16x32_f16 v[58:61], v[82:85], v[168:171], v[58:61]
	v_mfma_f32_16x16x32_f16 v[62:65], v[86:89], v[168:171], v[62:65]
	s_waitcnt lgkmcnt(1)
	v_mfma_f32_16x16x32_f16 v[66:69], v[82:85], v[156:159], v[66:69]
	v_mfma_f32_16x16x32_f16 v[70:73], v[86:89], v[156:159], v[70:73]
	s_waitcnt lgkmcnt(0)
	v_mfma_f32_16x16x32_f16 v[74:77], v[82:85], v[160:163], v[74:77]
	v_mfma_f32_16x16x32_f16 v[78:81], v[86:89], v[160:163], v[78:81]
	s_cbranch_vccnz .LBB4_111
	ds_read_b128 v[92:95], v146 offset:16384
	s_waitcnt lgkmcnt(0)
	v_mfma_f32_16x16x32_f16 v[6:9], v[82:85], v[92:95], v[6:9]
	v_mfma_f32_16x16x32_f16 v[2:5], v[86:89], v[92:95], v[2:5]

.LBB4_113:
	s_waitcnt lgkmcnt(0)
	v_add_u32_e32 v148, s35, v107
	ds_read_b128 v[82:85], v148
	ds_read_b128 v[86:89], v148 offset:2048
	v_add_u32_e32 v147, s35, v147
	ds_read_b128 v[92:95], v147
	ds_read_b128 v[96:99], v147 offset:2048
	ds_read_b128 v[156:159], v147 offset:4096
	ds_read_b128 v[160:163], v147 offset:6144
	ds_read_b128 v[164:167], v147 offset:8192
	ds_read_b128 v[168:171], v147 offset:10240
	s_and_b64 vcc, exec, s[24:25]
	s_waitcnt lgkmcnt(5)
	v_mfma_f32_16x16x32_f16 v[22:25], v[86:89], v[92:95], v[22:25]
	v_mfma_f32_16x16x32_f16 v[18:21], v[82:85], v[92:95], v[18:21]
	s_waitcnt lgkmcnt(4)
	v_mfma_f32_16x16x32_f16 v[26:29], v[82:85], v[96:99], v[26:29]
	v_mfma_f32_16x16x32_f16 v[30:33], v[86:89], v[96:99], v[30:33]
	s_waitcnt lgkmcnt(3)
	v_mfma_f32_16x16x32_f16 v[34:37], v[82:85], v[156:159], v[34:37]
	v_mfma_f32_16x16x32_f16 v[38:41], v[86:89], v[156:159], v[38:41]
	ds_read_b128 v[156:159], v147 offset:12288
	s_waitcnt lgkmcnt(3)
	v_mfma_f32_16x16x32_f16 v[42:45], v[82:85], v[160:163], v[42:45]
	v_mfma_f32_16x16x32_f16 v[46:49], v[86:89], v[160:163], v[46:49]
	ds_read_b128 v[160:163], v147 offset:14336
	s_waitcnt lgkmcnt(3)
	v_mfma_f32_16x16x32_f16 v[50:53], v[82:85], v[164:167], v[50:53]
	v_mfma_f32_16x16x32_f16 v[54:57], v[86:89], v[164:167], v[54:57]
	s_waitcnt lgkmcnt(2)
	v_mfma_f32_16x16x32_f16 v[58:61], v[82:85], v[168:171], v[58:61]
	v_mfma_f32_16x16x32_f16 v[62:65], v[86:89], v[168:171], v[62:65]
	s_waitcnt lgkmcnt(1)
	v_mfma_f32_16x16x32_f16 v[66:69], v[82:85], v[156:159], v[66:69]
	v_mfma_f32_16x16x32_f16 v[70:73], v[86:89], v[156:159], v[70:73]
	s_waitcnt lgkmcnt(0)
	v_mfma_f32_16x16x32_f16 v[74:77], v[82:85], v[160:163], v[74:77]
	v_mfma_f32_16x16x32_f16 v[78:81], v[86:89], v[160:163], v[78:81]
	s_cbranch_vccnz .LBB4_115
	ds_read_b128 v[92:95], v147 offset:16384
	s_waitcnt lgkmcnt(0)
	v_mfma_f32_16x16x32_f16 v[6:9], v[82:85], v[92:95], v[6:9]
	v_mfma_f32_16x16x32_f16 v[2:5], v[86:89], v[92:95], v[2:5]

.LBB4_121:
	s_mov_b64 s[30:31], 0x280
	v_readfirstlane_b32 s34, v144
	v_add_u32_e32 v174, 0x2000, v144
	v_lshl_add_u64 v[172:173], v[116:117], 0, s[30:31]
	s_mov_b32 m0, s34
	v_readfirstlane_b32 s34, v174
	v_add_u32_e32 v174, 0x4000, v144
	s_barrier
	s_waitcnt lgkmcnt(0)
	ds_read_b128 v[82:85], v138 offset:20480
	ds_read_b128 v[86:89], v138 offset:22528
	ds_read_b128 v[92:95], v137
	ds_read_b128 v[96:99], v137 offset:2048
	ds_read_b128 v[156:159], v137 offset:4096
	ds_read_b128 v[160:163], v137 offset:6144
	ds_read_b128 v[164:167], v137 offset:8192
	ds_read_b128 v[168:171], v137 offset:10240
	global_load_lds_dwordx4 v[172:173], off
	v_lshl_add_u64 v[172:173], v[114:115], 0, s[30:31]
	s_mov_b32 m0, s34
	v_readfirstlane_b32 s34, v174
	v_add_u32_e32 v174, 0x6000, v144
	global_load_lds_dwordx4 v[172:173], off
	v_lshl_add_u64 v[172:173], v[112:113], 0, s[30:31]
	s_mov_b32 m0, s34
	v_readfirstlane_b32 s34, v174
	global_load_lds_dwordx4 v[172:173], off
	v_lshl_add_u64 v[172:173], v[110:111], 0, s[30:31]
	s_mov_b32 m0, s34
	v_readfirstlane_b32 s34, v145
	v_add_u32_e32 v174, 0x2000, v145
	global_load_lds_dwordx4 v[172:173], off
	v_lshl_add_u64 v[172:173], v[120:121], 0, s[30:31]
	s_mov_b32 m0, s34
	v_readfirstlane_b32 s34, v174
	global_load_lds_dwordx4 v[172:173], off
	v_lshl_add_u64 v[172:173], v[118:119], 0, s[30:31]
	s_mov_b32 m0, s34
	s_and_b64 vcc, exec, s[14:15]
	global_load_lds_dwordx4 v[172:173], off
	s_cbranch_vccnz .LBB4_123
	v_lshl_add_u64 v[172:173], v[122:123], 0, s[30:31]
	s_add_i32 s30, 0, 0x1e000
	v_add_u32_e32 v174, s30, v1
	s_nop 0
	v_readfirstlane_b32 s30, v174
	s_mov_b32 m0, s30
	s_nop 0
	global_load_lds_dwordx4 v[172:173], off
.LBB4_123:
	s_and_b64 vcc, exec, s[24:25]
	s_waitcnt lgkmcnt(5)
	v_mfma_f32_16x16x32_f16 v[18:21], v[82:85], v[92:95], v[18:21]
	v_mfma_f32_16x16x32_f16 v[22:25], v[86:89], v[92:95], v[22:25]
	s_waitcnt lgkmcnt(4)
	v_mfma_f32_16x16x32_f16 v[26:29], v[82:85], v[96:99], v[26:29]
	v_mfma_f32_16x16x32_f16 v[30:33], v[86:89], v[96:99], v[30:33]
	s_waitcnt lgkmcnt(3)
	v_mfma_f32_16x16x32_f16 v[34:37], v[82:85], v[156:159], v[34:37]
	v_mfma_f32_16x16x32_f16 v[38:41], v[86:89], v[156:159], v[38:41]
	ds_read_b128 v[156:159], v137 offset:12288
	s_waitcnt lgkmcnt(3)
	v_mfma_f32_16x16x32_f16 v[42:45], v[82:85], v[160:163], v[42:45]
	v_mfma_f32_16x16x32_f16 v[46:49], v[86:89], v[160:163], v[46:49]
	ds_read_b128 v[160:163], v137 offset:14336
	s_waitcnt lgkmcnt(3)
	v_mfma_f32_16x16x32_f16 v[50:53], v[82:85], v[164:167], v[50:53]
	v_mfma_f32_16x16x32_f16 v[54:57], v[86:89], v[164:167], v[54:57]
	s_waitcnt lgkmcnt(2)
	v_mfma_f32_16x16x32_f16 v[58:61], v[82:85], v[168:171], v[58:61]
	v_mfma_f32_16x16x32_f16 v[62:65], v[86:89], v[168:171], v[62:65]
	s_waitcnt lgkmcnt(1)
	v_mfma_f32_16x16x32_f16 v[66:69], v[82:85], v[156:159], v[66:69]
	v_mfma_f32_16x16x32_f16 v[70:73], v[86:89], v[156:159], v[70:73]
	s_waitcnt lgkmcnt(0)
	v_mfma_f32_16x16x32_f16 v[74:77], v[82:85], v[160:163], v[74:77]
	v_mfma_f32_16x16x32_f16 v[78:81], v[86:89], v[160:163], v[78:81]
	s_cbranch_vccnz .LBB4_125
	ds_read_b128 v[92:95], v137 offset:16384
	s_waitcnt lgkmcnt(0)
	v_mfma_f32_16x16x32_f16 v[6:9], v[82:85], v[92:95], v[6:9]
	v_mfma_f32_16x16x32_f16 v[2:5], v[86:89], v[92:95], v[2:5]

.LBB4_127:
	s_waitcnt lgkmcnt(0)
	ds_read_b128 v[82:85], v139 offset:20480
	ds_read_b128 v[86:89], v139 offset:22528
	ds_read_b128 v[92:95], v0
	ds_read_b128 v[96:99], v0 offset:2048
	ds_read_b128 v[156:159], v0 offset:4096
	ds_read_b128 v[160:163], v0 offset:6144
	ds_read_b128 v[164:167], v0 offset:8192
	ds_read_b128 v[168:171], v0 offset:10240
	s_and_b64 vcc, exec, s[24:25]
	s_waitcnt lgkmcnt(5)
	v_mfma_f32_16x16x32_f16 v[18:21], v[82:85], v[92:95], v[18:21]
	v_mfma_f32_16x16x32_f16 v[22:25], v[86:89], v[92:95], v[22:25]
	s_waitcnt lgkmcnt(4)
	v_mfma_f32_16x16x32_f16 v[26:29], v[82:85], v[96:99], v[26:29]
	v_mfma_f32_16x16x32_f16 v[30:33], v[86:89], v[96:99], v[30:33]
	s_waitcnt lgkmcnt(3)
	v_mfma_f32_16x16x32_f16 v[34:37], v[82:85], v[156:159], v[34:37]
	v_mfma_f32_16x16x32_f16 v[38:41], v[86:89], v[156:159], v[38:41]
	ds_read_b128 v[156:159], v0 offset:12288
	s_waitcnt lgkmcnt(3)
	v_mfma_f32_16x16x32_f16 v[42:45], v[82:85], v[160:163], v[42:45]
	v_mfma_f32_16x16x32_f16 v[46:49], v[86:89], v[160:163], v[46:49]
	ds_read_b128 v[160:163], v0 offset:14336
	s_waitcnt lgkmcnt(3)
	v_mfma_f32_16x16x32_f16 v[50:53], v[82:85], v[164:167], v[50:53]
	v_mfma_f32_16x16x32_f16 v[54:57], v[86:89], v[164:167], v[54:57]
	s_waitcnt lgkmcnt(2)
	v_mfma_f32_16x16x32_f16 v[58:61], v[82:85], v[168:171], v[58:61]
	v_mfma_f32_16x16x32_f16 v[62:65], v[86:89], v[168:171], v[62:65]
	s_waitcnt lgkmcnt(1)
	v_mfma_f32_16x16x32_f16 v[66:69], v[82:85], v[156:159], v[66:69]
	v_mfma_f32_16x16x32_f16 v[70:73], v[86:89], v[156:159], v[70:73]
	s_waitcnt lgkmcnt(0)
	v_mfma_f32_16x16x32_f16 v[74:77], v[82:85], v[160:163], v[74:77]
	v_mfma_f32_16x16x32_f16 v[78:81], v[86:89], v[160:163], v[78:81]
	s_cbranch_vccz .LBB4_192
	s_and_b64 vcc, exec, s[26:27]
	s_cbranch_vccz .LBB4_193

.LBB4_132:
	v_add_u32_e32 v174, 0x5000, v135
	s_mov_b64 s[30:31], 0x300
	v_readfirstlane_b32 s34, v174
	v_add_u32_e32 v174, 0x7000, v135
	v_lshl_add_u64 v[172:173], v[116:117], 0, s[30:31]
	s_mov_b32 m0, s34
	v_readfirstlane_b32 s34, v174
	v_add_u32_e32 v174, 0x9000, v135
	s_barrier
	s_waitcnt lgkmcnt(0)
	ds_read_b128 v[82:85], v142 offset:53248
	ds_read_b128 v[86:89], v142 offset:55296
	ds_read_b128 v[92:95], v137 offset:53248
	ds_read_b128 v[96:99], v137 offset:55296
	ds_read_b128 v[156:159], v137 offset:57344
	ds_read_b128 v[160:163], v137 offset:59392
	ds_read_b128 v[164:167], v137 offset:61440
	ds_read_b128 v[168:171], v137 offset:63488
	global_load_lds_dwordx4 v[172:173], off
	v_lshl_add_u64 v[172:173], v[114:115], 0, s[30:31]
	s_mov_b32 m0, s34
	v_readfirstlane_b32 s34, v174
	v_add_u32_e32 v174, 0xb000, v135
	global_load_lds_dwordx4 v[172:173], off
	v_lshl_add_u64 v[172:173], v[112:113], 0, s[30:31]
	s_mov_b32 m0, s34
	v_readfirstlane_b32 s34, v174
	global_load_lds_dwordx4 v[172:173], off
	v_lshl_add_u64 v[172:173], v[110:111], 0, s[30:31]
	s_mov_b32 m0, s34
	v_readfirstlane_b32 s34, v135
	v_add_u32_e32 v174, 0x2000, v135
	global_load_lds_dwordx4 v[172:173], off
	v_lshl_add_u64 v[172:173], v[120:121], 0, s[30:31]
	s_mov_b32 m0, s34
	v_readfirstlane_b32 s34, v174
	global_load_lds_dwordx4 v[172:173], off
	v_lshl_add_u64 v[172:173], v[118:119], 0, s[30:31]
	s_mov_b32 m0, s34
	s_and_b64 vcc, exec, s[14:15]
	global_load_lds_dwordx4 v[172:173], off
	s_cbranch_vccnz .LBB4_134
	v_add_u32_e32 v174, 0x4000, v135
	v_lshl_add_u64 v[172:173], v[122:123], 0, s[30:31]
	v_readfirstlane_b32 s30, v174
	s_mov_b32 m0, s30
	s_nop 0
	global_load_lds_dwordx4 v[172:173], off
.LBB4_134:
	s_and_b64 vcc, exec, s[24:25]
	s_waitcnt lgkmcnt(5)
	v_mfma_f32_16x16x32_f16 v[18:21], v[82:85], v[92:95], v[18:21]
	v_mfma_f32_16x16x32_f16 v[22:25], v[86:89], v[92:95], v[22:25]
	s_waitcnt lgkmcnt(4)
	v_mfma_f32_16x16x32_f16 v[26:29], v[82:85], v[96:99], v[26:29]
	v_mfma_f32_16x16x32_f16 v[30:33], v[86:89], v[96:99], v[30:33]
	s_waitcnt lgkmcnt(3)
	v_mfma_f32_16x16x32_f16 v[34:37], v[82:85], v[156:159], v[34:37]
	v_mfma_f32_16x16x32_f16 v[38:41], v[86:89], v[156:159], v[38:41]
	ds_read_b128 v[156:159], v140 offset:12288
	s_waitcnt lgkmcnt(3)
	v_mfma_f32_16x16x32_f16 v[42:45], v[82:85], v[160:163], v[42:45]
	v_mfma_f32_16x16x32_f16 v[46:49], v[86:89], v[160:163], v[46:49]
	ds_read_b128 v[160:163], v140 offset:14336
	s_waitcnt lgkmcnt(3)
	v_mfma_f32_16x16x32_f16 v[50:53], v[82:85], v[164:167], v[50:53]
	v_mfma_f32_16x16x32_f16 v[54:57], v[86:89], v[164:167], v[54:57]
	s_waitcnt lgkmcnt(2)
	v_mfma_f32_16x16x32_f16 v[58:61], v[82:85], v[168:171], v[58:61]
	v_mfma_f32_16x16x32_f16 v[62:65], v[86:89], v[168:171], v[62:65]
	s_waitcnt lgkmcnt(1)
	v_mfma_f32_16x16x32_f16 v[66:69], v[82:85], v[156:159], v[66:69]
	v_mfma_f32_16x16x32_f16 v[70:73], v[86:89], v[156:159], v[70:73]
	s_waitcnt lgkmcnt(0)
	v_mfma_f32_16x16x32_f16 v[74:77], v[82:85], v[160:163], v[74:77]
	v_mfma_f32_16x16x32_f16 v[78:81], v[86:89], v[160:163], v[78:81]
	s_cbranch_vccnz .LBB4_136
	ds_read_b128 v[92:95], v140 offset:16384
	s_waitcnt lgkmcnt(0)
	v_mfma_f32_16x16x32_f16 v[6:9], v[82:85], v[92:95], v[6:9]
	v_mfma_f32_16x16x32_f16 v[2:5], v[86:89], v[92:95], v[2:5]

.LBB4_138:
	s_waitcnt lgkmcnt(0)
	ds_read_b128 v[82:85], v143 offset:53248
	ds_read_b128 v[86:89], v143 offset:55296
	ds_read_b128 v[92:95], v0 offset:53248
	ds_read_b128 v[96:99], v0 offset:55296
	ds_read_b128 v[156:159], v0 offset:57344
	ds_read_b128 v[160:163], v0 offset:59392
	ds_read_b128 v[164:167], v0 offset:61440
	ds_read_b128 v[168:171], v0 offset:63488
	s_and_b64 vcc, exec, s[24:25]
	s_waitcnt lgkmcnt(5)
	v_mfma_f32_16x16x32_f16 v[18:21], v[82:85], v[92:95], v[18:21]
	v_mfma_f32_16x16x32_f16 v[22:25], v[86:89], v[92:95], v[22:25]
	s_waitcnt lgkmcnt(4)
	v_mfma_f32_16x16x32_f16 v[26:29], v[82:85], v[96:99], v[26:29]
	v_mfma_f32_16x16x32_f16 v[30:33], v[86:89], v[96:99], v[30:33]
	s_waitcnt lgkmcnt(3)
	v_mfma_f32_16x16x32_f16 v[34:37], v[82:85], v[156:159], v[34:37]
	v_mfma_f32_16x16x32_f16 v[38:41], v[86:89], v[156:159], v[38:41]
	ds_read_b128 v[156:159], v141 offset:12288
	s_waitcnt lgkmcnt(3)
	v_mfma_f32_16x16x32_f16 v[42:45], v[82:85], v[160:163], v[42:45]
	v_mfma_f32_16x16x32_f16 v[46:49], v[86:89], v[160:163], v[46:49]
	ds_read_b128 v[160:163], v141 offset:14336
	s_waitcnt lgkmcnt(3)
	v_mfma_f32_16x16x32_f16 v[50:53], v[82:85], v[164:167], v[50:53]
	v_mfma_f32_16x16x32_f16 v[54:57], v[86:89], v[164:167], v[54:57]
	s_waitcnt lgkmcnt(2)
	v_mfma_f32_16x16x32_f16 v[58:61], v[82:85], v[168:171], v[58:61]
	v_mfma_f32_16x16x32_f16 v[62:65], v[86:89], v[168:171], v[62:65]
	s_waitcnt lgkmcnt(1)
	v_mfma_f32_16x16x32_f16 v[66:69], v[82:85], v[156:159], v[66:69]
	v_mfma_f32_16x16x32_f16 v[70:73], v[86:89], v[156:159], v[70:73]
	s_waitcnt lgkmcnt(0)
	v_mfma_f32_16x16x32_f16 v[74:77], v[82:85], v[160:163], v[74:77]
	v_mfma_f32_16x16x32_f16 v[78:81], v[86:89], v[160:163], v[78:81]
	s_cbranch_vccz .LBB4_195
	s_and_b64 vcc, exec, s[26:27]
	s_cbranch_vccz .LBB4_196

.LBB4_145:
	s_waitcnt lgkmcnt(0)
	ds_read_b128 v[114:117], v90
	ds_read_b128 v[118:121], v90 offset:2048
	ds_read_b128 v[82:85], v146
	ds_read_b128 v[86:89], v146 offset:2048
	ds_read_b128 v[156:159], v146 offset:4096
	ds_read_b128 v[160:163], v146 offset:6144
	ds_read_b128 v[164:167], v146 offset:8192
	ds_read_b128 v[168:171], v146 offset:10240
	s_and_b64 vcc, exec, s[24:25]
	s_waitcnt lgkmcnt(5)
	v_mfma_f32_16x16x32_f16 v[18:21], v[114:117], v[82:85], v[18:21]
	v_mfma_f32_16x16x32_f16 v[22:25], v[118:121], v[82:85], v[22:25]
	s_waitcnt lgkmcnt(4)
	v_mfma_f32_16x16x32_f16 v[26:29], v[114:117], v[86:89], v[26:29]
	v_mfma_f32_16x16x32_f16 v[30:33], v[118:121], v[86:89], v[30:33]
	s_waitcnt lgkmcnt(2)
	v_mfma_f32_16x16x32_f16 v[42:45], v[114:117], v[160:163], v[42:45]
	v_mfma_f32_16x16x32_f16 v[46:49], v[118:121], v[160:163], v[46:49]
	v_mfma_f32_16x16x32_f16 v[34:37], v[114:117], v[156:159], v[34:37]
	v_mfma_f32_16x16x32_f16 v[38:41], v[118:121], v[156:159], v[38:41]
	ds_read_b128 v[156:159], v146 offset:12288
	ds_read_b128 v[160:163], v146 offset:14336
	s_waitcnt lgkmcnt(3)
	v_mfma_f32_16x16x32_f16 v[82:85], v[114:117], v[164:167], v[50:53]
	v_mfma_f32_16x16x32_f16 v[86:89], v[118:121], v[164:167], v[54:57]
	s_nop 1
	s_waitcnt lgkmcnt(2)
	v_mfma_f32_16x16x32_f16 v[90:93], v[114:117], v[168:171], v[58:61]
	v_mfma_f32_16x16x32_f16 v[94:97], v[118:121], v[168:171], v[62:65]
	s_waitcnt lgkmcnt(1)
	v_mfma_f32_16x16x32_f16 v[98:101], v[114:117], v[156:159], v[66:69]
	v_mfma_f32_16x16x32_f16 v[102:105], v[118:121], v[156:159], v[70:73]
	s_waitcnt lgkmcnt(0)
	v_mfma_f32_16x16x32_f16 v[106:109], v[114:117], v[160:163], v[74:77]
	v_mfma_f32_16x16x32_f16 v[110:113], v[118:121], v[160:163], v[78:81]
	s_cbranch_vccnz .LBB4_147
	ds_read_b128 v[50:53], v146 offset:16384
	s_waitcnt lgkmcnt(0)
	v_mfma_f32_16x16x32_f16 v[6:9], v[114:117], v[50:53], v[6:9]
	v_mfma_f32_16x16x32_f16 v[2:5], v[118:121], v[50:53], v[2:5]

.LBB4_149:
	s_waitcnt lgkmcnt(0)
	ds_read_b128 v[114:117], v148
	ds_read_b128 v[118:121], v148 offset:2048
	ds_read_b128 v[54:57], v147
	ds_read_b128 v[58:61], v147 offset:2048
	ds_read_b128 v[156:159], v147 offset:4096
	ds_read_b128 v[160:163], v147 offset:6144
	ds_read_b128 v[164:167], v147 offset:8192
	ds_read_b128 v[168:171], v147 offset:10240
	s_and_b64 vcc, exec, s[24:25]
	s_waitcnt lgkmcnt(5)
	v_mfma_f32_16x16x32_f16 v[50:53], v[114:117], v[54:57], v[18:21]
	v_mfma_f32_16x16x32_f16 v[54:57], v[118:121], v[54:57], v[22:25]
	s_waitcnt lgkmcnt(4)
	v_mfma_f32_16x16x32_f16 v[18:21], v[114:117], v[58:61], v[26:29]
	v_mfma_f32_16x16x32_f16 v[22:25], v[118:121], v[58:61], v[30:33]
	s_nop 1
	s_waitcnt lgkmcnt(3)
	v_mfma_f32_16x16x32_f16 v[58:61], v[114:117], v[156:159], v[34:37]
	v_mfma_f32_16x16x32_f16 v[62:65], v[118:121], v[156:159], v[38:41]
	ds_read_b128 v[156:159], v147 offset:12288
	s_nop 1
	s_waitcnt lgkmcnt(3)
	v_mfma_f32_16x16x32_f16 v[26:29], v[114:117], v[160:163], v[42:45]
	v_mfma_f32_16x16x32_f16 v[30:33], v[118:121], v[160:163], v[46:49]
	ds_read_b128 v[160:163], v147 offset:14336
	s_nop 1
	s_waitcnt lgkmcnt(3)
	v_mfma_f32_16x16x32_f16 v[66:69], v[114:117], v[164:167], v[82:85]
	v_mfma_f32_16x16x32_f16 v[70:73], v[118:121], v[164:167], v[86:89]
	s_waitcnt lgkmcnt(2)
	v_mfma_f32_16x16x32_f16 v[34:37], v[114:117], v[168:171], v[90:93]
	v_mfma_f32_16x16x32_f16 v[38:41], v[118:121], v[168:171], v[94:97]
	s_waitcnt lgkmcnt(1)
	v_mfma_f32_16x16x32_f16 v[74:77], v[114:117], v[156:159], v[98:101]
	v_mfma_f32_16x16x32_f16 v[78:81], v[118:121], v[156:159], v[102:105]
	s_waitcnt lgkmcnt(0)
	v_mfma_f32_16x16x32_f16 v[42:45], v[114:117], v[160:163], v[106:109]
	v_mfma_f32_16x16x32_f16 v[46:49], v[118:121], v[160:163], v[110:113]
	s_cbranch_vccz .LBB4_198
	s_and_b64 vcc, exec, s[26:27]
	s_cbranch_vccz .LBB4_199

.LBB4_154:
	s_barrier
	s_waitcnt lgkmcnt(0)
	ds_read_b128 v[82:85], v138 offset:20480
	ds_read_b128 v[86:89], v138 offset:22528
	ds_read_b128 v[90:93], v137
	s_and_b64 vcc, exec, s[24:25]
	s_waitcnt lgkmcnt(0)
	v_mfma_f32_16x16x32_f16 v[50:53], v[82:85], v[90:93], v[50:53]
	v_mfma_f32_16x16x32_f16 v[54:57], v[86:89], v[90:93], v[54:57]
	ds_read_b128 v[90:93], v137 offset:2048
	ds_read_b128 v[156:159], v137 offset:4096
	ds_read_b128 v[160:163], v137 offset:6144
	ds_read_b128 v[164:167], v137 offset:8192
	ds_read_b128 v[168:171], v137 offset:10240
	s_waitcnt lgkmcnt(4)
	v_mfma_f32_16x16x32_f16 v[18:21], v[82:85], v[90:93], v[18:21]
	v_mfma_f32_16x16x32_f16 v[22:25], v[86:89], v[90:93], v[22:25]
	s_waitcnt lgkmcnt(3)
	v_mfma_f32_16x16x32_f16 v[58:61], v[82:85], v[156:159], v[58:61]
	v_mfma_f32_16x16x32_f16 v[62:65], v[86:89], v[156:159], v[62:65]
	ds_read_b128 v[156:159], v137 offset:12288
	s_waitcnt lgkmcnt(3)
	v_mfma_f32_16x16x32_f16 v[26:29], v[82:85], v[160:163], v[26:29]
	v_mfma_f32_16x16x32_f16 v[30:33], v[86:89], v[160:163], v[30:33]
	ds_read_b128 v[160:163], v137 offset:14336
	s_waitcnt lgkmcnt(3)
	v_mfma_f32_16x16x32_f16 v[66:69], v[82:85], v[164:167], v[66:69]
	v_mfma_f32_16x16x32_f16 v[70:73], v[86:89], v[164:167], v[70:73]
	s_waitcnt lgkmcnt(2)
	v_mfma_f32_16x16x32_f16 v[34:37], v[82:85], v[168:171], v[34:37]
	v_mfma_f32_16x16x32_f16 v[38:41], v[86:89], v[168:171], v[38:41]
	s_waitcnt lgkmcnt(1)
	v_mfma_f32_16x16x32_f16 v[74:77], v[82:85], v[156:159], v[74:77]
	v_mfma_f32_16x16x32_f16 v[78:81], v[86:89], v[156:159], v[78:81]
	s_waitcnt lgkmcnt(0)
	v_mfma_f32_16x16x32_f16 v[42:45], v[82:85], v[160:163], v[42:45]
	v_mfma_f32_16x16x32_f16 v[46:49], v[86:89], v[160:163], v[46:49]
	s_cbranch_vccnz .LBB4_156
	ds_read_b128 v[90:93], v137 offset:16384
	s_waitcnt lgkmcnt(0)
	v_mfma_f32_16x16x32_f16 v[6:9], v[82:85], v[90:93], v[6:9]
	v_mfma_f32_16x16x32_f16 v[2:5], v[86:89], v[90:93], v[2:5]

.LBB4_158:
	s_waitcnt lgkmcnt(0)
	ds_read_b128 v[82:85], v139 offset:20480
	ds_read_b128 v[86:89], v139 offset:22528
	ds_read_b128 v[90:93], v0
	ds_read_b128 v[94:97], v0 offset:2048
	ds_read_b128 v[156:159], v0 offset:4096
	ds_read_b128 v[160:163], v0 offset:6144
	ds_read_b128 v[164:167], v0 offset:8192
	ds_read_b128 v[168:171], v0 offset:10240
	s_and_b64 vcc, exec, s[24:25]
	s_waitcnt lgkmcnt(5)
	v_mfma_f32_16x16x32_f16 v[50:53], v[82:85], v[90:93], v[50:53]
	v_mfma_f32_16x16x32_f16 v[54:57], v[86:89], v[90:93], v[54:57]
	s_waitcnt lgkmcnt(4)
	v_mfma_f32_16x16x32_f16 v[18:21], v[82:85], v[94:97], v[18:21]
	v_mfma_f32_16x16x32_f16 v[22:25], v[86:89], v[94:97], v[22:25]
	s_waitcnt lgkmcnt(3)
	v_mfma_f32_16x16x32_f16 v[58:61], v[82:85], v[156:159], v[58:61]
	v_mfma_f32_16x16x32_f16 v[62:65], v[86:89], v[156:159], v[62:65]
	ds_read_b128 v[156:159], v0 offset:12288
	s_waitcnt lgkmcnt(3)
	v_mfma_f32_16x16x32_f16 v[26:29], v[82:85], v[160:163], v[26:29]
	v_mfma_f32_16x16x32_f16 v[30:33], v[86:89], v[160:163], v[30:33]
	ds_read_b128 v[160:163], v0 offset:14336
	s_waitcnt lgkmcnt(3)
	v_mfma_f32_16x16x32_f16 v[66:69], v[82:85], v[164:167], v[66:69]
	v_mfma_f32_16x16x32_f16 v[70:73], v[86:89], v[164:167], v[70:73]
	s_waitcnt lgkmcnt(2)
	v_mfma_f32_16x16x32_f16 v[34:37], v[82:85], v[168:171], v[34:37]
	v_mfma_f32_16x16x32_f16 v[38:41], v[86:89], v[168:171], v[38:41]
	s_waitcnt lgkmcnt(1)
	v_mfma_f32_16x16x32_f16 v[74:77], v[82:85], v[156:159], v[74:77]
	v_mfma_f32_16x16x32_f16 v[78:81], v[86:89], v[156:159], v[78:81]
	s_waitcnt lgkmcnt(0)
	v_mfma_f32_16x16x32_f16 v[42:45], v[82:85], v[160:163], v[42:45]
	v_mfma_f32_16x16x32_f16 v[46:49], v[86:89], v[160:163], v[46:49]
	s_cbranch_vccnz .LBB4_160
	ds_read_b128 v[90:93], v0 offset:16384
	s_waitcnt lgkmcnt(0)
	v_mfma_f32_16x16x32_f16 v[6:9], v[82:85], v[90:93], v[6:9]
	v_mfma_f32_16x16x32_f16 v[2:5], v[86:89], v[90:93], v[2:5]

.LBB4_162:
	s_waitcnt vmcnt(0)
	s_barrier
	s_waitcnt lgkmcnt(0)
	ds_read_b128 v[114:117], v142 offset:53248
	ds_read_b128 v[118:121], v142 offset:55296
	ds_read_b128 v[82:85], v137 offset:53248
	s_and_b64 vcc, exec, s[24:25]
	s_waitcnt lgkmcnt(0)
	v_mfma_f32_16x16x32_f16 v[50:53], v[114:117], v[82:85], v[50:53]
	v_mfma_f32_16x16x32_f16 v[54:57], v[118:121], v[82:85], v[54:57]
	ds_read_b128 v[82:85], v137 offset:55296
	ds_read_b128 v[156:159], v137 offset:57344
	ds_read_b128 v[160:163], v137 offset:59392
	ds_read_b128 v[164:167], v137 offset:63488
	ds_read_b128 v[168:171], v137 offset:61440
	s_waitcnt lgkmcnt(4)
	v_mfma_f32_16x16x32_f16 v[98:101], v[118:121], v[82:85], v[22:25]
	s_nop 2
	v_mfma_f32_16x16x32_f16 v[94:97], v[114:117], v[82:85], v[18:21]
	s_waitcnt lgkmcnt(3)
	v_mfma_f32_16x16x32_f16 v[18:21], v[114:117], v[156:159], v[58:61]
	s_nop 2
	s_waitcnt lgkmcnt(2)
	v_mfma_f32_16x16x32_f16 v[102:105], v[114:117], v[160:163], v[26:29]
	v_mfma_f32_16x16x32_f16 v[106:109], v[118:121], v[160:163], v[30:33]
	ds_read_b128 v[160:163], v140 offset:12288
	s_nop 1
	s_waitcnt lgkmcnt(2)
	v_mfma_f32_16x16x32_f16 v[34:37], v[114:117], v[164:167], v[34:37]
	v_mfma_f32_16x16x32_f16 v[38:41], v[118:121], v[164:167], v[38:41]
	ds_read_b128 v[164:167], v140 offset:14336
	s_waitcnt lgkmcnt(1)
	v_mfma_f32_16x16x32_f16 v[82:85], v[114:117], v[160:163], v[74:77]
	v_mfma_f32_16x16x32_f16 v[86:89], v[118:121], v[160:163], v[78:81]
	v_mfma_f32_16x16x32_f16 v[22:25], v[118:121], v[156:159], v[62:65]
	v_mfma_f32_16x16x32_f16 v[26:29], v[114:117], v[168:171], v[66:69]
	v_mfma_f32_16x16x32_f16 v[30:33], v[118:121], v[168:171], v[70:73]
	s_waitcnt lgkmcnt(0)
	v_mfma_f32_16x16x32_f16 v[110:113], v[114:117], v[164:167], v[42:45]
	v_mfma_f32_16x16x32_f16 v[90:93], v[118:121], v[164:167], v[46:49]
	s_cbranch_vccnz .LBB4_164
	s_nop 0
	ds_read_b128 v[42:45], v140 offset:16384
	s_waitcnt lgkmcnt(0)
	v_mfma_f32_16x16x32_f16 v[6:9], v[114:117], v[42:45], v[6:9]
	v_mfma_f32_16x16x32_f16 v[2:5], v[118:121], v[42:45], v[2:5]

	.amdhsa_kernel _Z8moe_gemmILi2EEvPKDF16_S1_PvPKyPKiPKfS1_
		.amdhsa_group_segment_fixed_size 0
		.amdhsa_private_segment_fixed_size 0
		.amdhsa_kernarg_size 56
		.amdhsa_user_sgpr_count 2
		.amdhsa_user_sgpr_dispatch_ptr 0
		.amdhsa_user_sgpr_queue_ptr 0
		.amdhsa_user_sgpr_kernarg_segment_ptr 1
		.amdhsa_user_sgpr_dispatch_id 0
		.amdhsa_user_sgpr_kernarg_preload_length 0
		.amdhsa_user_sgpr_kernarg_preload_offset 0
		.amdhsa_user_sgpr_private_segment_size 0
		.amdhsa_uses_dynamic_stack 0
		.amdhsa_enable_private_segment 0
		.amdhsa_system_sgpr_workgroup_id_x 1
		.amdhsa_system_sgpr_workgroup_id_y 0
		.amdhsa_system_sgpr_workgroup_id_z 0
		.amdhsa_system_sgpr_workgroup_info 0
		.amdhsa_system_vgpr_workitem_id 0
		.amdhsa_next_free_vgpr 176
		.amdhsa_next_free_sgpr 62
		.amdhsa_accum_offset 176
		.amdhsa_reserve_vcc 1
		.amdhsa_float_round_mode_32 0
		.amdhsa_float_round_mode_16_64 0
		.amdhsa_float_denorm_mode_32 3
		.amdhsa_float_denorm_mode_16_64 3
		.amdhsa_dx10_clamp 1
		.amdhsa_ieee_mode 1
		.amdhsa_fp16_overflow 0
		.amdhsa_tg_split 0
		.amdhsa_exception_fp_ieee_invalid_op 0
		.amdhsa_exception_fp_denorm_src 0
		.amdhsa_exception_fp_ieee_div_zero 0
		.amdhsa_exception_fp_ieee_overflow 0
		.amdhsa_exception_fp_ieee_underflow 0
		.amdhsa_exception_fp_ieee_inexact 0
		.amdhsa_exception_int_div_zero 0
	.end_amdhsa_kernel

amdhsa.kernels:
  - .agpr_count:     0
    .args:
      - .actual_access:  write_only
        .address_space:  global
        .offset:         0
        .size:           8
        .value_kind:     global_buffer
    .group_segment_fixed_size: 0
    .kernarg_segment_align: 8
    .kernarg_segment_size: 8
    .language:       OpenCL C
    .language_version:
      - 2
      - 0
    .max_flat_workgroup_size: 1024
    .name:           _Z15zero_cnt_kernelPy
    .private_segment_fixed_size: 0
    .sgpr_count:     10
    .sgpr_spill_count: 0
    .symbol:         _Z15zero_cnt_kernelPy.kd
    .uniform_work_group_size: 1
    .uses_dynamic_stack: false
    .vgpr_count:     3
    .vgpr_spill_count: 0
    .wavefront_size: 64
  - .agpr_count:     0
    .args:
      - .actual_access:  read_only
        .address_space:  global
        .offset:         0
        .size:           8
        .value_kind:     global_buffer
      - .actual_access:  read_only
        .address_space:  global
        .offset:         8
        .size:           8
        .value_kind:     global_buffer
      - .actual_access:  read_only
        .address_space:  global
        .offset:         16
        .size:           8
        .value_kind:     global_buffer
      - .actual_access:  read_only
        .address_space:  global
        .offset:         24
        .size:           8
        .value_kind:     global_buffer
      - .actual_access:  write_only
        .address_space:  global
        .offset:         32
        .size:           8
        .value_kind:     global_buffer
      - .actual_access:  write_only
        .address_space:  global
        .offset:         40
        .size:           8
        .value_kind:     global_buffer
      - .actual_access:  write_only
        .address_space:  global
        .offset:         48
        .size:           8
        .value_kind:     global_buffer
      - .address_space:  global
        .offset:         56
        .size:           8
        .value_kind:     global_buffer
      - .actual_access:  write_only
        .address_space:  global
        .offset:         64
        .size:           8
        .value_kind:     global_buffer
      - .actual_access:  write_only
        .address_space:  global
        .offset:         72
        .size:           8
        .value_kind:     global_buffer
    .group_segment_fixed_size: 0
    .kernarg_segment_align: 8
    .kernarg_segment_size: 80
    .language:       OpenCL C
    .language_version:
      - 2
      - 0
    .max_flat_workgroup_size: 256
    .name:           _Z11prep_kernelPKfS0_S0_S0_PDF16_S1_S1_PyPiPf
    .private_segment_fixed_size: 0
    .sgpr_count:     55
    .sgpr_spill_count: 0
    .symbol:         _Z11prep_kernelPKfS0_S0_S0_PDF16_S1_S1_PyPiPf.kd
    .uniform_work_group_size: 1
    .uses_dynamic_stack: false
    .vgpr_count:     248
    .vgpr_spill_count: 0
    .wavefront_size: 64
  - .agpr_count:     0
    .args:
      - .address_space:  global
        .offset:         0
        .size:           8
        .value_kind:     global_buffer
      - .address_space:  global
        .offset:         8
        .size:           8
        .value_kind:     global_buffer
      - .actual_access:  write_only
        .address_space:  global
        .offset:         16
        .size:           8
        .value_kind:     global_buffer
      - .actual_access:  read_only
        .address_space:  global
        .offset:         24
        .size:           8
        .value_kind:     global_buffer
      - .actual_access:  read_only
        .address_space:  global
        .offset:         32
        .size:           8
        .value_kind:     global_buffer
      - .actual_access:  read_only
        .address_space:  global
        .offset:         40
        .size:           8
        .value_kind:     global_buffer
      - .actual_access:  read_only
        .address_space:  global
        .offset:         48
        .size:           8
        .value_kind:     global_buffer
    .group_segment_fixed_size: 0
    .kernarg_segment_align: 8
    .kernarg_segment_size: 56
    .language:       OpenCL C
    .language_version:
      - 2
      - 0
    .max_flat_workgroup_size: 512
    .name:           _Z8moe_gemmILi0EEvPKDF16_S1_PvPKyPKiPKfS1_
    .private_segment_fixed_size: 0
    .sgpr_count:     82
    .sgpr_spill_count: 0
    .symbol:         _Z8moe_gemmILi0EEvPKDF16_S1_PvPKyPKiPKfS1_.kd
    .uniform_work_group_size: 1
    .uses_dynamic_stack: false
    .vgpr_count:     252
    .vgpr_spill_count: 0
    .wavefront_size: 64
  - .agpr_count:     0
    .args:
      - .address_space:  global
        .offset:         0
        .size:           8
        .value_kind:     global_buffer
      - .address_space:  global
        .offset:         8
        .size:           8
        .value_kind:     global_buffer
      - .actual_access:  write_only
        .address_space:  global
        .offset:         16
        .size:           8
        .value_kind:     global_buffer
      - .actual_access:  read_only
        .address_space:  global
        .offset:         24
        .size:           8
        .value_kind:     global_buffer
      - .actual_access:  read_only
        .address_space:  global
        .offset:         32
        .size:           8
        .value_kind:     global_buffer
      - .actual_access:  read_only
        .address_space:  global
        .offset:         40
        .size:           8
        .value_kind:     global_buffer
      - .actual_access:  read_only
        .address_space:  global
        .offset:         48
        .size:           8
        .value_kind:     global_buffer
    .group_segment_fixed_size: 0
    .kernarg_segment_align: 8
    .kernarg_segment_size: 56
    .language:       OpenCL C
    .language_version:
      - 2
      - 0
    .max_flat_workgroup_size: 512
    .name:           _Z8moe_gemmILi1EEvPKDF16_S1_PvPKyPKiPKfS1_
    .private_segment_fixed_size: 0
    .sgpr_count:     68
    .sgpr_spill_count: 0
    .symbol:         _Z8moe_gemmILi1EEvPKDF16_S1_PvPKyPKiPKfS1_.kd
    .uniform_work_group_size: 1
    .uses_dynamic_stack: false
    .vgpr_count:     168
    .vgpr_spill_count: 0
    .wavefront_size: 64
  - .agpr_count:     0
    .args:
      - .address_space:  global
        .offset:         0
        .size:           8
        .value_kind:     global_buffer
      - .address_space:  global
        .offset:         8
        .size:           8
        .value_kind:     global_buffer
      - .actual_access:  write_only
        .address_space:  global
        .offset:         16
        .size:           8
        .value_kind:     global_buffer
      - .actual_access:  read_only
        .address_space:  global
        .offset:         24
        .size:           8
        .value_kind:     global_buffer
      - .actual_access:  read_only
        .address_space:  global
        .offset:         32
        .size:           8
        .value_kind:     global_buffer
      - .actual_access:  read_only
        .address_space:  global
        .offset:         40
        .size:           8
        .value_kind:     global_buffer
      - .actual_access:  read_only
        .address_space:  global
        .offset:         48
        .size:           8
        .value_kind:     global_buffer
    .group_segment_fixed_size: 0
    .kernarg_segment_align: 8
    .kernarg_segment_size: 56
    .language:       OpenCL C
    .language_version:
      - 2
      - 0
    .max_flat_workgroup_size: 512
    .name:           _Z8moe_gemmILi2EEvPKDF16_S1_PvPKyPKiPKfS1_
    .private_segment_fixed_size: 0
    .sgpr_count:     68
    .sgpr_spill_count: 0
    .symbol:         _Z8moe_gemmILi2EEvPKDF16_S1_PvPKyPKiPKfS1_.kd
    .uniform_work_group_size: 1
    .uses_dynamic_stack: false
    .vgpr_count:     176
    .vgpr_spill_count: 0
    .wavefront_size: 64
